# gathers: priority stays raised through the per-token epilogue and next-token preamble (serial reductions), dropping again at the first bulk decode
# baseline (speedup 1.0000x reference)
.LBB0_763:
	s_cmpk_ge_i32 s58, 0x70
	s_cselect_b64 s[12:13], -1, 0
	ds_bpermute_b32 v84, v93, v92
	s_and_b64 vcc, s[12:13], s[48:49]
	v_cndmask_b32_e32 v104, v0, v94, vcc
	v_ashrrev_i32_e32 v105, 31, v104
	s_add_i32 s12, s58, 16
	s_and_b32 s12, s12, 0x70
	v_lshlrev_b64 v[104:105], 9, v[104:105]
	v_lshl_add_u64 v[104:105], s[94:95], 0, v[104:105]
	s_lshl_b32 s36, s12, 2
	s_waitcnt lgkmcnt(0)
	s_waitcnt vmcnt(32)
	v_mov_b32_e32 v92, v122
	v_ashrrev_i32_e32 v85, 31, v84
	v_lshl_add_u64 v[104:105], v[104:105], 0, s[36:37]
	v_lshl_add_u64 v[84:85], v[84:85], 3, s[8:9]
	v_lshl_add_u64 v[104:105], v[104:105], 0, v[144:145]
	global_load_dwordx2 v[84:85], v[84:85], off
	s_nop 0
	global_load_dword v86, v[72:73], off
	global_load_dword v122, v[104:105], off
	s_waitcnt vmcnt(19)
	v_dot8_i32_i4 v87, v8, v1, 0
	v_dot8_i32_i4 v104, v8, v88, 0
	v_dot8_i32_i4 v87, v9, v89, v87
	v_dot8_i32_i4 v104, v9, v90, v104
	s_waitcnt vmcnt(19)
	v_dot8_i32_i4 v9, v10, v88, 0
	v_dot8_i32_i4 v9, v11, v90, v9
	v_lshl_add_u32 v87, v87, 4, v104
	v_dot8_i32_i4 v8, v10, v1, 0
	v_dot8_i32_i4 v8, v11, v89, v8
	s_add_i32 s58, s58, 16
	v_lshl_add_u64 v[72:73], v[72:73], 0, 64
	s_nop 0
	v_lshl_add_u32 v104, v8, 4, v9
	v_dot8_i32_i4 v8, v12, v1, 0
	v_dot8_i32_i4 v9, v12, v88, 0
	v_dot8_i32_i4 v8, v13, v89, v8
	v_dot8_i32_i4 v9, v13, v90, v9
	v_readlane_b32 s12, v92, 0
	v_readlane_b32 s28, v92, 8
	v_readlane_b32 s30, v92, 9
	v_lshl_add_u32 v105, v8, 4, v9
	v_dot8_i32_i4 v8, v14, v1, 0
	v_dot8_i32_i4 v9, v14, v88, 0
	v_dot8_i32_i4 v8, v15, v89, v8
	v_dot8_i32_i4 v9, v15, v90, v9
	s_ashr_i32 s13, s12, 31
	v_readlane_b32 s14, v92, 1
	s_ashr_i32 s29, s28, 31
	v_lshl_add_u32 v106, v8, 4, v9
	v_dot8_i32_i4 v8, v16, v1, 0
	v_dot8_i32_i4 v9, v16, v88, 0
	v_dot8_i32_i4 v8, v17, v89, v8
	v_dot8_i32_i4 v9, v17, v90, v9
	s_ashr_i32 s31, s30, 31
	v_readlane_b32 s34, v92, 10
	s_lshl_b64 s[12:13], s[12:13], 9
	v_lshl_add_u32 v107, v8, 4, v9
	v_dot8_i32_i4 v8, v18, v1, 0
	v_dot8_i32_i4 v9, v18, v88, 0
	v_dot8_i32_i4 v8, v19, v89, v8
	v_dot8_i32_i4 v9, v19, v90, v9
	s_ashr_i32 s15, s14, 31
	v_readlane_b32 s16, v92, 2
	s_lshl_b64 s[28:29], s[28:29], 9
	v_lshl_add_u32 v108, v8, 4, v9
	v_dot8_i32_i4 v8, v20, v1, 0
	v_dot8_i32_i4 v9, v20, v88, 0
	v_dot8_i32_i4 v8, v21, v89, v8
	v_dot8_i32_i4 v9, v21, v90, v9
	s_lshl_b64 s[30:31], s[30:31], 9
	s_ashr_i32 s35, s34, 31
	v_readlane_b32 s38, v92, 11
	v_lshl_add_u32 v109, v8, 4, v9
	v_dot8_i32_i4 v8, v22, v1, 0
	v_dot8_i32_i4 v9, v22, v88, 0
	v_dot8_i32_i4 v8, v23, v89, v8
	v_dot8_i32_i4 v9, v23, v90, v9
	s_lshl_b64 s[14:15], s[14:15], 9
	s_ashr_i32 s17, s16, 31
	v_readlane_b32 s18, v92, 3
	v_lshl_add_u32 v110, v8, 4, v9
	v_dot8_i32_i4 v8, v24, v1, 0
	v_dot8_i32_i4 v9, v24, v88, 0
	v_dot8_i32_i4 v8, v25, v89, v8
	v_dot8_i32_i4 v9, v25, v90, v9
	s_lshl_b64 s[34:35], s[34:35], 9
	s_ashr_i32 s39, s38, 31
	s_nop 0
	v_lshl_add_u32 v111, v8, 4, v9
	v_dot8_i32_i4 v8, v38, v1, 0
	v_dot8_i32_i4 v9, v38, v88, 0
	v_dot8_i32_i4 v8, v39, v89, v8
	v_dot8_i32_i4 v9, v39, v90, v9
	s_setprio 2
	v_permlane32_swap_b32 v87, v111
	s_nop 1
	v_lshl_add_u32 v112, v8, 4, v9
	v_dot8_i32_i4 v8, v50, v1, 0
	v_dot8_i32_i4 v9, v50, v88, 0
	v_dot8_i32_i4 v8, v51, v89, v8
	v_dot8_i32_i4 v9, v51, v90, v9
	s_waitcnt lgkmcnt(0)
	v_add_u32_e32 v87, v87, v111
	v_permlane32_swap_b32 v104, v112
	v_lshl_add_u32 v113, v8, 4, v9
	v_dot8_i32_i4 v8, v48, v1, 0
	v_dot8_i32_i4 v9, v48, v88, 0
	v_dot8_i32_i4 v8, v49, v89, v8
	v_dot8_i32_i4 v9, v49, v90, v9
	s_waitcnt lgkmcnt(0)
	v_add_u32_e32 v104, v104, v112
	v_permlane32_swap_b32 v105, v113
	v_lshl_add_u32 v114, v8, 4, v9
	v_dot8_i32_i4 v8, v46, v1, 0
	v_dot8_i32_i4 v9, v46, v88, 0
	v_dot8_i32_i4 v8, v47, v89, v8
	v_dot8_i32_i4 v9, v47, v90, v9
	s_waitcnt lgkmcnt(0)
	v_add_u32_e32 v105, v105, v113
	v_permlane32_swap_b32 v106, v114
	v_lshl_add_u32 v115, v8, 4, v9
	v_dot8_i32_i4 v8, v44, v1, 0
	v_dot8_i32_i4 v9, v44, v88, 0
	v_dot8_i32_i4 v8, v45, v89, v8
	v_dot8_i32_i4 v9, v45, v90, v9
	s_waitcnt lgkmcnt(0)
	v_add_u32_e32 v106, v106, v114
	v_permlane32_swap_b32 v107, v115
	v_lshl_add_u32 v116, v8, 4, v9
	v_dot8_i32_i4 v8, v42, v1, 0
	v_dot8_i32_i4 v9, v42, v88, 0
	v_dot8_i32_i4 v8, v43, v89, v8
	v_dot8_i32_i4 v9, v43, v90, v9
	s_waitcnt lgkmcnt(0)
	v_add_u32_e32 v107, v107, v115
	v_permlane32_swap_b32 v108, v116
	v_lshl_add_u32 v117, v8, 4, v9
	v_dot8_i32_i4 v8, v40, v1, 0
	v_dot8_i32_i4 v9, v40, v88, 0
	v_dot8_i32_i4 v8, v41, v89, v8
	v_dot8_i32_i4 v9, v41, v90, v9
	s_waitcnt lgkmcnt(0)
	v_add_u32_e32 v108, v108, v116
	v_permlane32_swap_b32 v109, v117
	v_lshl_add_u32 v118, v8, 4, v9
	s_waitcnt lgkmcnt(0)
	v_add_u32_e32 v109, v109, v117
	v_permlane32_swap_b32 v110, v118
	v_readlane_b32 s50, v92, 12
	s_lshl_b64 s[16:17], s[16:17], 9
	s_ashr_i32 s19, s18, 31
	s_waitcnt lgkmcnt(0)
	v_add_u32_e32 v110, v110, v118
	v_permlane16_swap_b32 v87, v107
	v_readlane_b32 s20, v92, 4
	s_add_u32 s66, s28, s62
	s_addc_u32 s67, s29, s63
	global_load_dwordx2 v[24:25], v121, s[66:67]
	s_add_u32 s66, s30, s62
	s_addc_u32 s67, s31, s63
	global_load_dwordx2 v[38:39], v121, s[66:67]
	s_waitcnt lgkmcnt(0)
	v_add_u32_e32 v87, v87, v107
	v_permlane16_swap_b32 v104, v108
	s_lshl_b64 s[38:39], s[38:39], 9
	s_ashr_i32 s51, s50, 31
	v_readlane_b32 s52, v92, 13
	s_waitcnt lgkmcnt(0)
	v_add_u32_e32 v104, v104, v108
	v_permlane16_swap_b32 v105, v109
	s_lshl_b64 s[18:19], s[18:19], 9
	s_ashr_i32 s21, s20, 31
	v_readlane_b32 s22, v92, 5
	s_waitcnt lgkmcnt(0)
	v_add_u32_e32 v105, v105, v109
	v_permlane16_swap_b32 v106, v110
	s_add_u32 s66, s34, s62
	s_addc_u32 s67, s35, s63
	global_load_dwordx2 v[50:51], v121, s[66:67]
	s_lshl_b64 s[50:51], s[50:51], 9
	s_ashr_i32 s53, s52, 31
	s_waitcnt lgkmcnt(0)
	v_add_u32_e32 v106, v106, v110
	v_cndmask_b32_e64 v107, v87, v105, s[44:45]
	v_cndmask_b32_e64 v87, v105, v87, s[44:45]
	s_nop 0
	v_readlane_b32 s54, v92, 14
	s_lshl_b64 s[20:21], s[20:21], 9
	s_ashr_i32 s23, s22, 31
	v_readlane_b32 s24, v92, 6
	s_waitcnt lgkmcnt(0)
	v_add_u32_dpp v87, v107, v87 row_ror:8 row_mask:0xf bank_mask:0xf
	v_cndmask_b32_e64 v105, v104, v106, s[44:45]
	s_nop 1
	v_cndmask_b32_e64 v104, v106, v104, s[44:45]
	s_lshl_b64 s[52:53], s[52:53], 9
	s_ashr_i32 s55, s54, 31
	v_readlane_b32 s56, v92, 15
	s_waitcnt lgkmcnt(0)
	v_add_u32_dpp v104, v105, v104 row_ror:8 row_mask:0xf bank_mask:0xf
	v_cndmask_b32_e64 v105, v87, v104, s[46:47]
	v_cndmask_b32_e64 v87, v104, v87, s[46:47]
	s_nop 0
	v_mov_b32_dpp v104, v105 row_half_mirror row_mask:0xf bank_mask:0xf
	s_nop 1
	s_lshl_b64 s[22:23], s[22:23], 9
	s_ashr_i32 s25, s24, 31
	v_readlane_b32 s26, v92, 7
	s_lshl_b64 s[54:55], s[54:55], 9
	s_waitcnt lgkmcnt(0)
	v_add_u32_dpp v87, v104, v87 quad_perm:[3,2,1,0] row_mask:0xf bank_mask:0xf
	s_nop 1
	s_ashr_i32 s57, s56, 31
	s_lshl_b64 s[24:25], s[24:25], 9
	s_ashr_i32 s27, s26, 31
	s_lshl_b64 s[56:57], s[56:57], 9
	s_waitcnt lgkmcnt(0)
	v_add_u32_dpp v87, v87, v87 quad_perm:[2,3,0,1] row_mask:0xf bank_mask:0xf
	s_nop 1
	s_lshl_b64 s[26:27], s[26:27], 9
	s_add_u32 s66, s38, s62
	s_addc_u32 s67, s39, s63
	global_load_dwordx2 v[48:49], v121, s[66:67]
	s_add_u32 s66, s50, s62
	s_addc_u32 s67, s51, s63
	global_load_dwordx2 v[46:47], v121, s[66:67]
	s_add_u32 s66, s52, s62
	s_addc_u32 s67, s53, s63
	global_load_dwordx2 v[44:45], v121, s[66:67]
	s_add_u32 s66, s54, s62
	s_addc_u32 s67, s55, s63
	global_load_dwordx2 v[42:43], v121, s[66:67]
	s_add_u32 s66, s56, s62
	s_addc_u32 s67, s57, s63
	global_load_dwordx2 v[40:41], v121, s[66:67]
	s_add_u32 s66, s12, s62
	s_addc_u32 s67, s13, s63
	global_load_dwordx2 v[8:9], v121, s[66:67]
	s_add_u32 s66, s14, s62
	s_addc_u32 s67, s15, s63
	global_load_dwordx2 v[10:11], v121, s[66:67]
	s_add_u32 s66, s16, s62
	s_addc_u32 s67, s17, s63
	global_load_dwordx2 v[12:13], v121, s[66:67]
	s_add_u32 s66, s18, s62
	s_addc_u32 s67, s19, s63
	global_load_dwordx2 v[14:15], v121, s[66:67]
	s_add_u32 s66, s20, s62
	s_addc_u32 s67, s21, s63
	global_load_dwordx2 v[16:17], v121, s[66:67]
	s_add_u32 s66, s22, s62
	s_addc_u32 s67, s23, s63
	global_load_dwordx2 v[18:19], v121, s[66:67]
	s_add_u32 s66, s24, s62
	s_addc_u32 s67, s25, s63
	global_load_dwordx2 v[20:21], v121, s[66:67]
	s_add_u32 s66, s26, s62
	s_addc_u32 s67, s27, s63
	global_load_dwordx2 v[22:23], v121, s[66:67]
	s_waitcnt lgkmcnt(0)
	v_add_u32_dpp v87, v87, v87 quad_perm:[1,0,3,2] row_mask:0xf bank_mask:0xf
	s_waitcnt vmcnt(17)
	v_mul_f32_e32 v85, v91, v85
	v_cvt_f32_i32_e32 v87, v87
	v_add_f32_e32 v87, v95, v87
	v_mul_f32_e32 v85, v85, v87
	v_mul_f32_e32 v87, 0x3d372713, v85
	v_mul_f32_e32 v87, v85, v87
	v_fma_f32 v87, v85, v87, v85
	v_mul_f32_e32 v87, 0x3fcc422a, v87
	v_mul_f32_e32 v87, 0xbfb8aa3b, v87
	v_exp_f32_e32 v87, v87
	s_nop 0
	v_add_f32_e32 v87, 1.0, v87
	v_rcp_f32_e32 v87, v87
	s_nop 0
	v_pk_mul_f32 v[84:85], v[84:85], v[86:87]
	s_waitcnt vmcnt(34)
	v_alignbit_b32 v224, v82, v82, 4
	v_pk_mul_f32 v[84:85], v[84:85], v[84:85] op_sel:[0,1] op_sel_hi:[1,0]
	v_cvt_f16_f32_e32 v120, v84
	s_setprio 0
	v_and_b32_e32 v86, 0x7070707, v82
	v_readlane_b32 s36, v120, 0
	v_and_b32_e32 v87, 0x7070707, v224
	v_perm_b32 v86, s2, v205, v86
	v_perm_b32 v87, s2, v205, v87
	v_and_or_b32 v86, v82, s4, v86
	v_and_or_b32 v82, v224, s4, v87
	v_perm_b32 v87, v82, v86, s5
	v_perm_b32 v104, v82, v86, s33
	v_perm_b32 v105, v82, v86, s0
	v_perm_b32 v82, v82, v86, s1
	v_pk_fma_f16 v86, v87, s36, v103 op_sel_hi:[1,0,1]
	v_pk_fma_f16 v87, v104, s36, v102 op_sel_hi:[1,0,1]
	v_alignbit_b32 v225, v83, v83, 4
	v_pk_fma_f16 v82, v82, s36, v100 op_sel_hi:[1,0,1]
	v_and_b32_e32 v100, 0x7070707, v83
	v_and_b32_e32 v102, 0x7070707, v225
	v_perm_b32 v100, s2, v205, v100
	v_perm_b32 v102, s2, v205, v102
	v_and_or_b32 v100, v83, s4, v100
	v_and_or_b32 v83, v225, s4, v102
	v_perm_b32 v102, v83, v100, s5
	v_perm_b32 v103, v83, v100, s33
	v_perm_b32 v104, v83, v100, s0
	v_perm_b32 v83, v83, v100, s1
	v_readlane_b32 s59, v120, 4
	s_waitcnt vmcnt(33)
	v_alignbit_b32 v224, v80, v80, 4
	v_pk_fma_f16 v101, v105, s36, v101 op_sel_hi:[1,0,1]
	v_pk_fma_f16 v99, v102, s36, v99 op_sel_hi:[1,0,1]
	v_pk_fma_f16 v98, v103, s36, v98 op_sel_hi:[1,0,1]
	v_pk_fma_f16 v97, v104, s36, v97 op_sel_hi:[1,0,1]
	v_pk_fma_f16 v83, v83, s36, v96 op_sel_hi:[1,0,1]
	v_and_b32_e32 v96, 0x7070707, v80
	v_and_b32_e32 v100, 0x7070707, v224
	v_perm_b32 v96, s2, v205, v96
	v_perm_b32 v100, s2, v205, v100
	v_and_or_b32 v96, v80, s4, v96
	v_and_or_b32 v80, v224, s4, v100
	v_perm_b32 v100, v80, v96, s5
	v_perm_b32 v102, v80, v96, s33
	v_perm_b32 v103, v80, v96, s0
	v_perm_b32 v80, v80, v96, s1
	v_pk_fma_f16 v86, v100, s59, v86 op_sel_hi:[1,0,1]
	v_alignbit_b32 v225, v81, v81, 4
	v_pk_fma_f16 v80, v80, s59, v82 op_sel_hi:[1,0,1]
	v_and_b32_e32 v82, 0x7070707, v81
	v_and_b32_e32 v100, 0x7070707, v225
	v_pk_fma_f16 v96, v103, s59, v101 op_sel_hi:[1,0,1]
	v_perm_b32 v82, s2, v205, v82
	v_perm_b32 v100, s2, v205, v100
	v_and_or_b32 v82, v81, s4, v82
	v_and_or_b32 v81, v225, s4, v100
	v_perm_b32 v100, v81, v82, s5
	v_pk_fma_f16 v87, v102, s59, v87 op_sel_hi:[1,0,1]
	v_perm_b32 v101, v81, v82, s33
	v_perm_b32 v102, v81, v82, s0
	v_perm_b32 v81, v81, v82, s1
	v_pk_fma_f16 v82, v100, s59, v99 op_sel_hi:[1,0,1]
	v_readlane_b32 s60, v120, 8
	s_waitcnt vmcnt(32)
	v_alignbit_b32 v224, v78, v78, 4
	v_pk_fma_f16 v98, v101, s59, v98 op_sel_hi:[1,0,1]
	v_pk_fma_f16 v97, v102, s59, v97 op_sel_hi:[1,0,1]
	v_pk_fma_f16 v81, v81, s59, v83 op_sel_hi:[1,0,1]
	v_and_b32_e32 v85, 0x7070707, v78
	v_and_b32_e32 v99, 0x7070707, v224
	v_perm_b32 v85, s2, v205, v85
	v_perm_b32 v99, s2, v205, v99
	v_and_or_b32 v85, v78, s4, v85
	v_and_or_b32 v78, v224, s4, v99
	v_perm_b32 v99, v78, v85, s5
	v_perm_b32 v100, v78, v85, s33
	v_perm_b32 v101, v78, v85, s0
	v_perm_b32 v78, v78, v85, s1
	v_pk_fma_f16 v85, v99, s60, v86 op_sel_hi:[1,0,1]
	v_pk_fma_f16 v86, v100, s60, v87 op_sel_hi:[1,0,1]
	v_pk_fma_f16 v87, v101, s60, v96 op_sel_hi:[1,0,1]
	v_alignbit_b32 v225, v79, v79, 4
	v_pk_fma_f16 v78, v78, s60, v80 op_sel_hi:[1,0,1]
	v_and_b32_e32 v80, 0x7070707, v79
	v_and_b32_e32 v96, 0x7070707, v225
	v_perm_b32 v80, s2, v205, v80
	v_perm_b32 v96, s2, v205, v96
	v_and_or_b32 v80, v79, s4, v80
	v_and_or_b32 v79, v225, s4, v96
	v_perm_b32 v96, v79, v80, s5
	v_perm_b32 v100, v79, v80, s0
	v_perm_b32 v99, v79, v80, s33
	v_perm_b32 v79, v79, v80, s1
	v_pk_fma_f16 v80, v96, s60, v82 op_sel_hi:[1,0,1]
	v_pk_fma_f16 v96, v100, s60, v97 op_sel_hi:[1,0,1]
	v_readlane_b32 s36, v120, 12
	s_waitcnt vmcnt(31)
	v_alignbit_b32 v224, v76, v76, 4
	v_pk_fma_f16 v82, v99, s60, v98 op_sel_hi:[1,0,1]
	v_pk_fma_f16 v79, v79, s60, v81 op_sel_hi:[1,0,1]
	v_and_b32_e32 v83, 0x7070707, v76
	v_and_b32_e32 v97, 0x7070707, v224
	v_perm_b32 v83, s2, v205, v83
	v_perm_b32 v97, s2, v205, v97
	v_and_or_b32 v83, v76, s4, v83
	v_and_or_b32 v76, v224, s4, v97
	v_perm_b32 v97, v76, v83, s5
	v_perm_b32 v98, v76, v83, s33
	v_perm_b32 v99, v76, v83, s0
	v_perm_b32 v76, v76, v83, s1
	v_pk_fma_f16 v83, v97, s36, v85 op_sel_hi:[1,0,1]
	v_pk_fma_f16 v85, v98, s36, v86 op_sel_hi:[1,0,1]
	v_pk_fma_f16 v86, v99, s36, v87 op_sel_hi:[1,0,1]
	v_alignbit_b32 v225, v77, v77, 4
	v_pk_fma_f16 v76, v76, s36, v78 op_sel_hi:[1,0,1]
	v_and_b32_e32 v78, 0x7070707, v77
	v_and_b32_e32 v87, 0x7070707, v225
	v_perm_b32 v78, s2, v205, v78
	v_perm_b32 v87, s2, v205, v87
	v_and_or_b32 v78, v77, s4, v78
	v_and_or_b32 v77, v225, s4, v87
	v_perm_b32 v87, v77, v78, s5
	v_perm_b32 v97, v77, v78, s33
	v_perm_b32 v98, v77, v78, s0
	v_perm_b32 v77, v77, v78, s1
	v_pk_fma_f16 v78, v87, s36, v80 op_sel_hi:[1,0,1]
	v_readlane_b32 s59, v120, 16
	s_waitcnt vmcnt(30)
	v_alignbit_b32 v224, v74, v74, 4
	v_pk_fma_f16 v80, v97, s36, v82 op_sel_hi:[1,0,1]
	v_pk_fma_f16 v82, v98, s36, v96 op_sel_hi:[1,0,1]
	v_pk_fma_f16 v77, v77, s36, v79 op_sel_hi:[1,0,1]
	v_and_b32_e32 v81, 0x7070707, v74
	v_and_b32_e32 v87, 0x7070707, v224
	v_perm_b32 v81, s2, v205, v81
	v_perm_b32 v87, s2, v205, v87
	v_and_or_b32 v81, v74, s4, v81
	v_and_or_b32 v74, v224, s4, v87
	v_perm_b32 v87, v74, v81, s5
	v_perm_b32 v96, v74, v81, s33
	v_perm_b32 v97, v74, v81, s0
	v_perm_b32 v74, v74, v81, s1
	v_pk_fma_f16 v81, v87, s59, v83 op_sel_hi:[1,0,1]
	v_pk_fma_f16 v83, v96, s59, v85 op_sel_hi:[1,0,1]
	v_pk_fma_f16 v85, v97, s59, v86 op_sel_hi:[1,0,1]
	v_alignbit_b32 v225, v75, v75, 4
	v_pk_fma_f16 v74, v74, s59, v76 op_sel_hi:[1,0,1]
	v_and_b32_e32 v76, 0x7070707, v75
	v_and_b32_e32 v86, 0x7070707, v225
	v_perm_b32 v76, s2, v205, v76
	v_perm_b32 v86, s2, v205, v86
	v_and_or_b32 v76, v75, s4, v76
	v_and_or_b32 v75, v225, s4, v86
	v_perm_b32 v86, v75, v76, s5
	v_perm_b32 v87, v75, v76, s33
	v_perm_b32 v96, v75, v76, s0
	v_perm_b32 v75, v75, v76, s1
	v_pk_fma_f16 v76, v86, s59, v78 op_sel_hi:[1,0,1]
	v_pk_fma_f16 v78, v87, s59, v80 op_sel_hi:[1,0,1]
	v_pk_fma_f16 v80, v96, s59, v82 op_sel_hi:[1,0,1]
	v_readlane_b32 s60, v120, 20
	s_waitcnt vmcnt(29)
	v_alignbit_b32 v224, v70, v70, 4
	v_pk_fma_f16 v75, v75, s59, v77 op_sel_hi:[1,0,1]
	v_and_b32_e32 v79, 0x7070707, v70
	v_and_b32_e32 v82, 0x7070707, v224
	v_perm_b32 v79, s2, v205, v79
	v_perm_b32 v82, s2, v205, v82
	v_and_or_b32 v79, v70, s4, v79
	v_and_or_b32 v70, v224, s4, v82
	v_perm_b32 v82, v70, v79, s5
	v_perm_b32 v86, v70, v79, s33
	v_perm_b32 v87, v70, v79, s0
	v_perm_b32 v70, v70, v79, s1
	v_pk_fma_f16 v79, v82, s60, v81 op_sel_hi:[1,0,1]
	v_pk_fma_f16 v81, v86, s60, v83 op_sel_hi:[1,0,1]
	v_alignbit_b32 v225, v71, v71, 4
	v_pk_fma_f16 v70, v70, s60, v74 op_sel_hi:[1,0,1]
	v_and_b32_e32 v74, 0x7070707, v71
	v_and_b32_e32 v83, 0x7070707, v225
	v_pk_fma_f16 v82, v87, s60, v85 op_sel_hi:[1,0,1]
	v_perm_b32 v74, s2, v205, v74
	v_perm_b32 v83, s2, v205, v83
	v_and_or_b32 v74, v71, s4, v74
	v_and_or_b32 v71, v225, s4, v83
	v_perm_b32 v83, v71, v74, s5
	v_perm_b32 v85, v71, v74, s33
	v_perm_b32 v86, v71, v74, s0
	v_perm_b32 v71, v71, v74, s1
	v_pk_fma_f16 v74, v83, s60, v76 op_sel_hi:[1,0,1]
	v_pk_fma_f16 v76, v85, s60, v78 op_sel_hi:[1,0,1]
	v_pk_fma_f16 v78, v86, s60, v80 op_sel_hi:[1,0,1]
	v_readlane_b32 s36, v120, 24
	s_waitcnt vmcnt(28)
	v_alignbit_b32 v224, v68, v68, 4
	v_pk_fma_f16 v71, v71, s60, v75 op_sel_hi:[1,0,1]
	v_and_b32_e32 v77, 0x7070707, v68
	v_and_b32_e32 v80, 0x7070707, v224
	v_perm_b32 v77, s2, v205, v77
	v_perm_b32 v80, s2, v205, v80
	v_and_or_b32 v77, v68, s4, v77
	v_and_or_b32 v68, v224, s4, v80
	v_perm_b32 v80, v68, v77, s5
	v_perm_b32 v83, v68, v77, s33
	v_perm_b32 v85, v68, v77, s0
	v_perm_b32 v68, v68, v77, s1
	v_pk_fma_f16 v77, v80, s36, v79 op_sel_hi:[1,0,1]
	v_pk_fma_f16 v79, v83, s36, v81 op_sel_hi:[1,0,1]
	v_alignbit_b32 v225, v69, v69, 4
	v_pk_fma_f16 v68, v68, s36, v70 op_sel_hi:[1,0,1]
	v_and_b32_e32 v70, 0x7070707, v69
	v_and_b32_e32 v81, 0x7070707, v225
	v_pk_fma_f16 v80, v85, s36, v82 op_sel_hi:[1,0,1]
	v_perm_b32 v70, s2, v205, v70
	v_perm_b32 v81, s2, v205, v81
	v_and_or_b32 v70, v69, s4, v70
	v_and_or_b32 v69, v225, s4, v81
	v_perm_b32 v81, v69, v70, s5
	v_perm_b32 v82, v69, v70, s33
	v_perm_b32 v83, v69, v70, s0
	v_perm_b32 v69, v69, v70, s1
	v_pk_fma_f16 v70, v81, s36, v74 op_sel_hi:[1,0,1]
	v_pk_fma_f16 v74, v82, s36, v76 op_sel_hi:[1,0,1]
	v_pk_fma_f16 v76, v83, s36, v78 op_sel_hi:[1,0,1]
	v_readlane_b32 s59, v120, 28
	s_waitcnt vmcnt(25)
	v_alignbit_b32 v224, v64, v64, 4
	v_pk_fma_f16 v69, v69, s36, v71 op_sel_hi:[1,0,1]
	v_and_b32_e32 v75, 0x7070707, v64
	v_and_b32_e32 v78, 0x7070707, v224
	v_perm_b32 v75, s2, v205, v75
	v_perm_b32 v78, s2, v205, v78
	v_and_or_b32 v75, v64, s4, v75
	v_and_or_b32 v64, v224, s4, v78
	v_perm_b32 v78, v64, v75, s5
	v_perm_b32 v81, v64, v75, s33
	v_perm_b32 v82, v64, v75, s0
	v_perm_b32 v64, v64, v75, s1
	v_pk_fma_f16 v75, v78, s59, v77 op_sel_hi:[1,0,1]
	v_pk_fma_f16 v77, v81, s59, v79 op_sel_hi:[1,0,1]
	v_alignbit_b32 v225, v65, v65, 4
	v_pk_fma_f16 v64, v64, s59, v68 op_sel_hi:[1,0,1]
	v_and_b32_e32 v68, 0x7070707, v65
	v_and_b32_e32 v79, 0x7070707, v225
	v_pk_fma_f16 v78, v82, s59, v80 op_sel_hi:[1,0,1]
	s_add_u32 s66, s12, s64
	s_addc_u32 s67, s13, s65
	global_load_dwordx2 v[82:83], v121, s[66:67]
	v_perm_b32 v68, s2, v205, v68
	v_perm_b32 v79, s2, v205, v79
	v_and_or_b32 v68, v65, s4, v68
	v_and_or_b32 v65, v225, s4, v79
	v_perm_b32 v79, v65, v68, s5
	v_perm_b32 v80, v65, v68, s33
	v_perm_b32 v81, v65, v68, s0
	v_perm_b32 v65, v65, v68, s1
	v_pk_fma_f16 v68, v79, s59, v70 op_sel_hi:[1,0,1]
	v_pk_fma_f16 v70, v80, s59, v74 op_sel_hi:[1,0,1]
	v_pk_fma_f16 v74, v81, s59, v76 op_sel_hi:[1,0,1]
	v_readlane_b32 s60, v120, 32
	s_waitcnt vmcnt(25)
	v_alignbit_b32 v224, v62, v62, 4
	v_pk_fma_f16 v65, v65, s59, v69 op_sel_hi:[1,0,1]
	v_and_b32_e32 v71, 0x7070707, v62
	v_and_b32_e32 v76, 0x7070707, v224
	v_perm_b32 v71, s2, v205, v71
	v_perm_b32 v76, s2, v205, v76
	v_and_or_b32 v71, v62, s4, v71
	v_and_or_b32 v62, v224, s4, v76
	v_perm_b32 v76, v62, v71, s5
	v_perm_b32 v79, v62, v71, s33
	v_perm_b32 v80, v62, v71, s0
	v_perm_b32 v62, v62, v71, s1
	v_pk_fma_f16 v71, v76, s60, v75 op_sel_hi:[1,0,1]
	v_pk_fma_f16 v75, v79, s60, v77 op_sel_hi:[1,0,1]
	v_alignbit_b32 v225, v63, v63, 4
	v_pk_fma_f16 v62, v62, s60, v64 op_sel_hi:[1,0,1]
	v_and_b32_e32 v64, 0x7070707, v63
	v_and_b32_e32 v77, 0x7070707, v225
	v_pk_fma_f16 v76, v80, s60, v78 op_sel_hi:[1,0,1]
	s_add_u32 s66, s14, s64
	s_addc_u32 s67, s15, s65
	global_load_dwordx2 v[80:81], v121, s[66:67]
	v_perm_b32 v64, s2, v205, v64
	v_perm_b32 v77, s2, v205, v77
	v_and_or_b32 v64, v63, s4, v64
	v_and_or_b32 v63, v225, s4, v77
	v_perm_b32 v77, v63, v64, s5
	v_perm_b32 v78, v63, v64, s33
	v_perm_b32 v79, v63, v64, s0
	v_perm_b32 v63, v63, v64, s1
	v_pk_fma_f16 v64, v77, s60, v68 op_sel_hi:[1,0,1]
	v_pk_fma_f16 v68, v78, s60, v70 op_sel_hi:[1,0,1]
	v_pk_fma_f16 v70, v79, s60, v74 op_sel_hi:[1,0,1]
	v_readlane_b32 s36, v120, 36
	s_waitcnt vmcnt(29)
	v_alignbit_b32 v224, v66, v66, 4
	v_pk_fma_f16 v63, v63, s60, v65 op_sel_hi:[1,0,1]
	v_and_b32_e32 v69, 0x7070707, v66
	v_and_b32_e32 v74, 0x7070707, v224
	v_perm_b32 v69, s2, v205, v69
	v_perm_b32 v74, s2, v205, v74
	v_and_or_b32 v69, v66, s4, v69
	v_and_or_b32 v66, v224, s4, v74
	v_perm_b32 v74, v66, v69, s5
	v_perm_b32 v77, v66, v69, s33
	v_perm_b32 v78, v66, v69, s0
	v_perm_b32 v66, v66, v69, s1
	v_pk_fma_f16 v69, v74, s36, v71 op_sel_hi:[1,0,1]
	v_pk_fma_f16 v71, v77, s36, v75 op_sel_hi:[1,0,1]
	v_alignbit_b32 v225, v67, v67, 4
	v_pk_fma_f16 v62, v66, s36, v62 op_sel_hi:[1,0,1]
	v_and_b32_e32 v66, 0x7070707, v67
	v_and_b32_e32 v75, 0x7070707, v225
	v_pk_fma_f16 v74, v78, s36, v76 op_sel_hi:[1,0,1]
	s_add_u32 s66, s16, s64
	s_addc_u32 s67, s17, s65
	global_load_dwordx2 v[78:79], v121, s[66:67]
	v_perm_b32 v66, s2, v205, v66
	v_perm_b32 v75, s2, v205, v75
	v_and_or_b32 v66, v67, s4, v66
	v_and_or_b32 v67, v225, s4, v75
	v_perm_b32 v76, v67, v66, s33
	v_perm_b32 v77, v67, v66, s0
	v_perm_b32 v75, v67, v66, s5
	v_perm_b32 v66, v67, v66, s1
	v_pk_fma_f16 v67, v76, s36, v68 op_sel_hi:[1,0,1]
	v_pk_fma_f16 v68, v77, s36, v70 op_sel_hi:[1,0,1]
	v_readlane_b32 s59, v120, 40
	s_waitcnt vmcnt(26)
	v_alignbit_b32 v224, v60, v60, 4
	v_pk_fma_f16 v64, v75, s36, v64 op_sel_hi:[1,0,1]
	v_pk_fma_f16 v63, v66, s36, v63 op_sel_hi:[1,0,1]
	v_and_b32_e32 v66, 0x7070707, v60
	v_and_b32_e32 v70, 0x7070707, v224
	v_perm_b32 v66, s2, v205, v66
	v_perm_b32 v70, s2, v205, v70
	v_and_or_b32 v66, v60, s4, v66
	v_and_or_b32 v60, v224, s4, v70
	v_perm_b32 v70, v60, v66, s5
	v_perm_b32 v75, v60, v66, s33
	v_perm_b32 v76, v60, v66, s0
	v_perm_b32 v60, v60, v66, s1
	v_pk_fma_f16 v66, v70, s59, v69 op_sel_hi:[1,0,1]
	v_pk_fma_f16 v69, v75, s59, v71 op_sel_hi:[1,0,1]
	v_alignbit_b32 v225, v61, v61, 4
	v_pk_fma_f16 v60, v60, s59, v62 op_sel_hi:[1,0,1]
	v_and_b32_e32 v62, 0x7070707, v61
	v_and_b32_e32 v71, 0x7070707, v225
	v_pk_fma_f16 v70, v76, s59, v74 op_sel_hi:[1,0,1]
	s_add_u32 s66, s18, s64
	s_addc_u32 s67, s19, s65
	global_load_dwordx2 v[76:77], v121, s[66:67]
	v_perm_b32 v62, s2, v205, v62
	v_perm_b32 v71, s2, v205, v71
	v_and_or_b32 v62, v61, s4, v62
	v_and_or_b32 v61, v225, s4, v71
	v_perm_b32 v71, v61, v62, s5
	v_perm_b32 v74, v61, v62, s33
	v_perm_b32 v75, v61, v62, s0
	v_perm_b32 v61, v61, v62, s1
	v_pk_fma_f16 v62, v71, s59, v64 op_sel_hi:[1,0,1]
	v_pk_fma_f16 v64, v74, s59, v67 op_sel_hi:[1,0,1]
	v_pk_fma_f16 v67, v75, s59, v68 op_sel_hi:[1,0,1]
	v_readlane_b32 s60, v120, 44
	s_waitcnt vmcnt(26)
	v_alignbit_b32 v224, v58, v58, 4
	v_pk_fma_f16 v61, v61, s59, v63 op_sel_hi:[1,0,1]
	v_and_b32_e32 v65, 0x7070707, v58
	v_and_b32_e32 v68, 0x7070707, v224
	v_perm_b32 v65, s2, v205, v65
	v_perm_b32 v68, s2, v205, v68
	v_and_or_b32 v65, v58, s4, v65
	v_and_or_b32 v58, v224, s4, v68
	v_perm_b32 v68, v58, v65, s5
	v_perm_b32 v71, v58, v65, s33
	v_perm_b32 v74, v58, v65, s0
	v_perm_b32 v58, v58, v65, s1
	v_pk_fma_f16 v65, v68, s60, v66 op_sel_hi:[1,0,1]
	v_pk_fma_f16 v66, v71, s60, v69 op_sel_hi:[1,0,1]
	v_alignbit_b32 v225, v59, v59, 4
	v_pk_fma_f16 v58, v58, s60, v60 op_sel_hi:[1,0,1]
	v_and_b32_e32 v60, 0x7070707, v59
	v_and_b32_e32 v69, 0x7070707, v225
	v_pk_fma_f16 v68, v74, s60, v70 op_sel_hi:[1,0,1]
	s_add_u32 s66, s20, s64
	s_addc_u32 s67, s21, s65
	global_load_dwordx2 v[74:75], v121, s[66:67]
	v_perm_b32 v60, s2, v205, v60
	v_perm_b32 v69, s2, v205, v69
	v_and_or_b32 v60, v59, s4, v60
	v_and_or_b32 v59, v225, s4, v69
	v_perm_b32 v69, v59, v60, s5
	v_perm_b32 v70, v59, v60, s33
	v_perm_b32 v71, v59, v60, s0
	v_perm_b32 v59, v59, v60, s1
	v_pk_fma_f16 v60, v69, s60, v62 op_sel_hi:[1,0,1]
	v_pk_fma_f16 v62, v70, s60, v64 op_sel_hi:[1,0,1]
	v_pk_fma_f16 v64, v71, s60, v67 op_sel_hi:[1,0,1]
	v_readlane_b32 s36, v120, 48
	s_waitcnt vmcnt(26)
	v_alignbit_b32 v224, v56, v56, 4
	v_pk_fma_f16 v59, v59, s60, v61 op_sel_hi:[1,0,1]
	v_and_b32_e32 v63, 0x7070707, v56
	v_and_b32_e32 v67, 0x7070707, v224
	v_perm_b32 v63, s2, v205, v63
	v_perm_b32 v67, s2, v205, v67
	v_and_or_b32 v63, v56, s4, v63
	v_and_or_b32 v56, v224, s4, v67
	v_perm_b32 v67, v56, v63, s5
	v_perm_b32 v69, v56, v63, s33
	v_perm_b32 v70, v56, v63, s0
	v_perm_b32 v56, v56, v63, s1
	v_pk_fma_f16 v63, v67, s36, v65 op_sel_hi:[1,0,1]
	v_alignbit_b32 v225, v57, v57, 4
	v_pk_fma_f16 v56, v56, s36, v58 op_sel_hi:[1,0,1]
	v_and_b32_e32 v58, 0x7070707, v57
	v_and_b32_e32 v67, 0x7070707, v225
	v_pk_fma_f16 v65, v69, s36, v66 op_sel_hi:[1,0,1]
	v_pk_fma_f16 v66, v70, s36, v68 op_sel_hi:[1,0,1]
	s_add_u32 s66, s22, s64
	s_addc_u32 s67, s23, s65
	global_load_dwordx2 v[70:71], v121, s[66:67]
	v_perm_b32 v58, s2, v205, v58
	v_perm_b32 v67, s2, v205, v67
	v_and_or_b32 v58, v57, s4, v58
	v_and_or_b32 v57, v225, s4, v67
	v_perm_b32 v67, v57, v58, s5
	v_perm_b32 v68, v57, v58, s33
	v_perm_b32 v69, v57, v58, s0
	v_perm_b32 v57, v57, v58, s1
	v_pk_fma_f16 v58, v67, s36, v60 op_sel_hi:[1,0,1]
	v_pk_fma_f16 v60, v68, s36, v62 op_sel_hi:[1,0,1]
	v_pk_fma_f16 v62, v69, s36, v64 op_sel_hi:[1,0,1]
	v_readlane_b32 s59, v120, 52
	s_waitcnt vmcnt(26)
	v_alignbit_b32 v224, v54, v54, 4
	v_pk_fma_f16 v57, v57, s36, v59 op_sel_hi:[1,0,1]
	v_and_b32_e32 v61, 0x7070707, v54
	v_and_b32_e32 v64, 0x7070707, v224
	v_perm_b32 v61, s2, v205, v61
	v_perm_b32 v64, s2, v205, v64
	v_and_or_b32 v61, v54, s4, v61
	v_and_or_b32 v54, v224, s4, v64
	v_perm_b32 v64, v54, v61, s5
	v_perm_b32 v67, v54, v61, s33
	v_perm_b32 v68, v54, v61, s0
	v_perm_b32 v54, v54, v61, s1
	v_pk_fma_f16 v61, v64, s59, v63 op_sel_hi:[1,0,1]
	v_pk_fma_f16 v63, v67, s59, v65 op_sel_hi:[1,0,1]
	v_alignbit_b32 v225, v55, v55, 4
	v_pk_fma_f16 v54, v54, s59, v56 op_sel_hi:[1,0,1]
	v_and_b32_e32 v56, 0x7070707, v55
	v_and_b32_e32 v65, 0x7070707, v225
	v_pk_fma_f16 v64, v68, s59, v66 op_sel_hi:[1,0,1]
	s_add_u32 s66, s24, s64
	s_addc_u32 s67, s25, s65
	global_load_dwordx2 v[68:69], v121, s[66:67]
	v_perm_b32 v56, s2, v205, v56
	v_perm_b32 v65, s2, v205, v65
	v_and_or_b32 v56, v55, s4, v56
	v_and_or_b32 v55, v225, s4, v65
	v_perm_b32 v65, v55, v56, s5
	v_perm_b32 v66, v55, v56, s33
	v_perm_b32 v67, v55, v56, s0
	v_perm_b32 v55, v55, v56, s1
	v_pk_fma_f16 v56, v65, s59, v58 op_sel_hi:[1,0,1]
	v_pk_fma_f16 v58, v66, s59, v60 op_sel_hi:[1,0,1]
	v_pk_fma_f16 v60, v67, s59, v62 op_sel_hi:[1,0,1]
	v_readlane_b32 s60, v120, 56
	s_waitcnt vmcnt(26)
	v_alignbit_b32 v224, v52, v52, 4
	v_pk_fma_f16 v55, v55, s59, v57 op_sel_hi:[1,0,1]
	v_and_b32_e32 v59, 0x7070707, v52
	v_and_b32_e32 v62, 0x7070707, v224
	v_perm_b32 v59, s2, v205, v59
	v_perm_b32 v62, s2, v205, v62
	v_and_or_b32 v59, v52, s4, v59
	v_and_or_b32 v52, v224, s4, v62
	v_perm_b32 v62, v52, v59, s5
	v_perm_b32 v65, v52, v59, s33
	v_perm_b32 v66, v52, v59, s0
	v_perm_b32 v52, v52, v59, s1
	v_pk_fma_f16 v59, v62, s60, v61 op_sel_hi:[1,0,1]
	v_pk_fma_f16 v61, v65, s60, v63 op_sel_hi:[1,0,1]
	v_alignbit_b32 v225, v53, v53, 4
	v_pk_fma_f16 v52, v52, s60, v54 op_sel_hi:[1,0,1]
	v_and_b32_e32 v54, 0x7070707, v53
	v_and_b32_e32 v63, 0x7070707, v225
	v_pk_fma_f16 v62, v66, s60, v64 op_sel_hi:[1,0,1]
	s_add_u32 s66, s30, s64
	s_addc_u32 s67, s31, s65
	global_load_dwordx2 v[66:67], v121, s[66:67]
	v_perm_b32 v54, s2, v205, v54
	v_perm_b32 v63, s2, v205, v63
	v_and_or_b32 v54, v53, s4, v54
	v_and_or_b32 v53, v225, s4, v63
	v_perm_b32 v63, v53, v54, s5
	v_perm_b32 v64, v53, v54, s33
	v_perm_b32 v65, v53, v54, s0
	v_perm_b32 v53, v53, v54, s1
	v_pk_fma_f16 v54, v63, s60, v56 op_sel_hi:[1,0,1]
	v_pk_fma_f16 v56, v64, s60, v58 op_sel_hi:[1,0,1]
	v_pk_fma_f16 v58, v65, s60, v60 op_sel_hi:[1,0,1]
	v_readlane_b32 s36, v120, 60
	s_waitcnt vmcnt(34)
	v_alignbit_b32 v224, v36, v36, 4
	v_pk_fma_f16 v53, v53, s60, v55 op_sel_hi:[1,0,1]
	v_and_b32_e32 v57, 0x7070707, v36
	v_and_b32_e32 v60, 0x7070707, v224
	v_perm_b32 v57, s2, v205, v57
	v_perm_b32 v60, s2, v205, v60
	v_and_or_b32 v57, v36, s4, v57
	v_and_or_b32 v36, v224, s4, v60
	v_perm_b32 v60, v36, v57, s5
	v_perm_b32 v63, v36, v57, s33
	v_perm_b32 v64, v36, v57, s0
	v_perm_b32 v36, v36, v57, s1
	v_pk_fma_f16 v100, v36, s36, v52 op_sel_hi:[1,0,1]
	v_alignbit_b32 v225, v37, v37, 4
	v_and_b32_e32 v36, 0x7070707, v37
	v_and_b32_e32 v52, 0x7070707, v225
	v_perm_b32 v36, s2, v205, v36
	v_perm_b32 v52, s2, v205, v52
	v_and_or_b32 v36, v37, s4, v36
	v_and_or_b32 v37, v225, s4, v52
	v_pk_fma_f16 v103, v60, s36, v59 op_sel_hi:[1,0,1]
	v_perm_b32 v52, v37, v36, s5
	v_perm_b32 v57, v37, v36, s33
	v_perm_b32 v59, v37, v36, s0
	v_perm_b32 v36, v37, v36, s1
	v_pk_fma_f16 v96, v36, s36, v53 op_sel_hi:[1,0,1]
	s_add_u32 s66, s56, s64
	s_addc_u32 s67, s57, s65
	global_load_dwordx2 v[36:37], v121, s[66:67]
	v_pk_fma_f16 v101, v64, s36, v62 op_sel_hi:[1,0,1]
	s_add_u32 s66, s26, s64
	s_addc_u32 s67, s27, s65
	global_load_dwordx2 v[64:65], v121, s[66:67]
	v_pk_fma_f16 v102, v63, s36, v61 op_sel_hi:[1,0,1]
	s_add_u32 s66, s28, s64
	s_addc_u32 s67, s29, s65
	global_load_dwordx2 v[62:63], v121, s[66:67]
	s_add_u32 s66, s34, s64
	s_addc_u32 s67, s35, s65
	global_load_dwordx2 v[60:61], v121, s[66:67]
	v_pk_fma_f16 v97, v59, s36, v58 op_sel_hi:[1,0,1]
	s_add_u32 s66, s38, s64
	s_addc_u32 s67, s39, s65
	global_load_dwordx2 v[58:59], v121, s[66:67]
	v_pk_fma_f16 v98, v57, s36, v56 op_sel_hi:[1,0,1]
	s_add_u32 s66, s50, s64
	s_addc_u32 s67, s51, s65
	global_load_dwordx2 v[56:57], v121, s[66:67]
	v_pk_fma_f16 v99, v52, s36, v54 op_sel_hi:[1,0,1]
	s_add_u32 s66, s52, s64
	s_addc_u32 s67, s53, s65
	global_load_dwordx2 v[54:55], v121, s[66:67]
	s_add_u32 s66, s54, s64
	s_addc_u32 s67, s55, s65
	global_load_dwordx2 v[52:53], v121, s[66:67]
	s_nop 0
	s_nop 0
	s_nop 0
	s_nop 0
	s_nop 0
	s_nop 0
	s_nop 0
	s_cmpk_eq_i32 s58, 0x90
	s_cbranch_scc0 .LBB0_763
	s_setprio 2
	v_lshlrev_b64 v[0:1], 2, v[2:3]
	v_lshl_add_u64 v[2:3], v[28:29], 0, v[0:1]
	v_mov_b32_e32 v104, v208
	v_mov_b32_e32 v105, v209
	v_mov_b32_e32 v106, v210
	v_mov_b32_e32 v107, v211
	v_mov_b32_e32 v108, v212
	v_mov_b32_e32 v109, v213
	v_mov_b32_e32 v110, v214
	v_mov_b32_e32 v111, v215
	v_mov_b32_e32 v86, v216
	v_mov_b32_e32 v87, v217
	v_mov_b32_e32 v88, v218
	v_mov_b32_e32 v89, v219
	v_mov_b32_e32 v112, v220
	v_mov_b32_e32 v113, v221
	v_mov_b32_e32 v114, v222
	v_mov_b32_e32 v115, v223
	v_lshl_add_u64 v[72:73], v[32:33], 0, v[0:1]
	v_cvt_f32_f16_sdwa v1, v103 dst_sel:DWORD dst_unused:UNUSED_PAD src0_sel:WORD_1
	v_cvt_f32_f16_e32 v0, v103
	v_cvt_f32_f16_sdwa v91, v102 dst_sel:DWORD dst_unused:UNUSED_PAD src0_sel:WORD_1
	v_cvt_f32_f16_e32 v90, v102
	v_cvt_f32_f16_sdwa v103, v101 dst_sel:DWORD dst_unused:UNUSED_PAD src0_sel:WORD_1
	v_cvt_f32_f16_e32 v102, v101
	v_cvt_f32_f16_sdwa v101, v100 dst_sel:DWORD dst_unused:UNUSED_PAD src0_sel:WORD_1
	v_cvt_f32_f16_e32 v100, v100
	s_mov_b32 s18, 0x800000
	v_readlane_b32 s12, v255, 5
	v_readlane_b32 s13, v255, 6
	v_pk_add_f32 v[86:87], v[86:87], v[102:103]
	v_pk_add_f32 v[84:85], v[112:113], v[0:1]
	v_mov_b32_e32 v102, v85
	v_mov_b32_e32 v103, v87
	v_pk_add_f32 v[90:91], v[114:115], v[90:91]
	v_pk_add_f32 v[88:89], v[88:89], v[100:101]
	v_mov_b32_e32 v100, v84
	v_mov_b32_e32 v101, v86
	v_pk_mul_f32 v[102:103], v[102:103], v[102:103]
	v_mov_b32_e32 v112, v91
	v_pk_fma_f32 v[100:101], v[100:101], v[100:101], v[102:103]
	v_mov_b32_e32 v102, v90
	v_mov_b32_e32 v103, v88
	v_pk_fma_f32 v[100:101], v[102:103], v[102:103], v[100:101]
	v_cvt_f32_f16_sdwa v103, v99 dst_sel:DWORD dst_unused:UNUSED_PAD src0_sel:WORD_1
	v_cvt_f32_f16_e32 v102, v99
	v_cvt_f32_f16_sdwa v99, v98 dst_sel:DWORD dst_unused:UNUSED_PAD src0_sel:WORD_1
	v_cvt_f32_f16_e32 v98, v98
	v_mov_b32_e32 v113, v89
	v_pk_add_f32 v[102:103], v[108:109], v[102:103]
	v_cvt_f32_f16_sdwa v109, v97 dst_sel:DWORD dst_unused:UNUSED_PAD src0_sel:WORD_1
	v_cvt_f32_f16_e32 v108, v97
	v_cvt_f32_f16_sdwa v97, v96 dst_sel:DWORD dst_unused:UNUSED_PAD src0_sel:WORD_1
	v_cvt_f32_f16_e32 v96, v96
	v_pk_add_f32 v[98:99], v[110:111], v[98:99]
	v_pk_add_f32 v[104:105], v[104:105], v[108:109]
	v_mov_b32_e32 v108, v103
	v_mov_b32_e32 v109, v105
	v_pk_add_f32 v[96:97], v[106:107], v[96:97]
	v_mov_b32_e32 v106, v102
	v_mov_b32_e32 v107, v104
	v_pk_mul_f32 v[108:109], v[108:109], v[108:109]
	v_pk_fma_f32 v[100:101], v[112:113], v[112:113], v[100:101]
	v_pk_fma_f32 v[106:107], v[106:107], v[106:107], v[108:109]
	v_mov_b32_e32 v108, v98
	v_mov_b32_e32 v109, v96
	v_mov_b32_e32 v110, v99
	v_mov_b32_e32 v111, v97
	v_pk_fma_f32 v[106:107], v[108:109], v[108:109], v[106:107]
	v_add_f32_e32 v95, v100, v101
	v_pk_fma_f32 v[106:107], v[110:111], v[110:111], v[106:107]
	v_lshl_add_u64 v[34:35], v[34:35], 0, s[12:13]
	v_add_f32_e32 v95, v95, v106
	v_add_f32_e32 v95, v95, v107
	v_mov_b32_e32 v100, v95
	s_nop 1
	v_permlane32_swap_b32 v100, v95
	s_waitcnt lgkmcnt(0)
	v_add_f32_e32 v95, v95, v100
	v_mov_b32_e32 v100, v95
	s_nop 1
	v_permlane16_swap_b32 v100, v95
	s_waitcnt lgkmcnt(0)
	v_add_f32_e32 v95, v95, v100
	s_nop 1
	v_mov_b32_dpp v100, v95 row_ror:8 row_mask:0xf bank_mask:0xf
	s_waitcnt lgkmcnt(0)
	v_add_f32_e32 v95, v95, v100
	s_nop 1
	v_mov_b32_dpp v100, v95 row_half_mirror row_mask:0xf bank_mask:0xf
	s_nop 1
	v_mov_b32_dpp v100, v100 quad_perm:[3,2,1,0] row_mask:0xf bank_mask:0xf
	s_waitcnt lgkmcnt(0)
	v_add_f32_e32 v95, v95, v100
	s_nop 1
	v_mov_b32_dpp v100, v95 quad_perm:[2,3,0,1] row_mask:0xf bank_mask:0xf
	s_waitcnt lgkmcnt(0)
	v_add_f32_e32 v95, v95, v100
	s_nop 1
	v_mov_b32_dpp v100, v95 quad_perm:[1,0,3,2] row_mask:0xf bank_mask:0xf
	s_waitcnt lgkmcnt(0)
	v_add_f32_e32 v95, v95, v100
	v_fmamk_f32 v95, v95, 0x3a800000, v191
	v_cmp_gt_f32_e32 vcc, s18, v95
	v_mul_f32_e32 v100, 0x4b800000, v95
	s_nop 0
	v_cndmask_b32_e32 v95, v95, v100, vcc
	v_rsq_f32_e32 v95, v95
	s_nop 0
	v_mul_f32_e32 v100, 0x45800000, v95
	v_cndmask_b32_e32 v100, v95, v100, vcc
	v_pk_mul_f32 v[84:85], v[84:85], v[100:101] op_sel_hi:[1,0]
	v_pk_mul_f32 v[0:1], v[124:125], v[84:85]
	v_pk_mul_f32 v[84:85], v[90:91], v[100:101] op_sel_hi:[1,0]
	s_nop 0
	v_pk_mul_f32 v[2:3], v[126:127], v[84:85]
	global_store_dwordx4 v[72:73], v[0:3], off
	s_nop 1
	v_pk_mul_f32 v[84:85], v[86:87], v[100:101] op_sel_hi:[1,0]
	v_pk_mul_f32 v[0:1], v[128:129], v[84:85]
	v_pk_mul_f32 v[84:85], v[88:89], v[100:101] op_sel_hi:[1,0]
	s_nop 0
	v_pk_mul_f32 v[2:3], v[130:131], v[84:85]
	global_store_dwordx4 v[72:73], v[0:3], off offset:16
	s_nop 1
	v_pk_mul_f32 v[84:85], v[102:103], v[100:101] op_sel_hi:[1,0]
	v_pk_mul_f32 v[0:1], v[84:85], v[132:133]
	v_pk_mul_f32 v[84:85], v[98:99], v[100:101] op_sel_hi:[1,0]
	s_nop 0
	v_pk_mul_f32 v[2:3], v[84:85], v[134:135]
	global_store_dwordx4 v[72:73], v[0:3], off offset:32
	s_nop 1
	v_pk_mul_f32 v[84:85], v[104:105], v[100:101] op_sel_hi:[1,0]
	v_pk_mul_f32 v[0:1], v[84:85], v[136:137]
	v_pk_mul_f32 v[84:85], v[96:97], v[100:101] op_sel_hi:[1,0]
	s_nop 0
	v_pk_mul_f32 v[2:3], v[84:85], v[138:139]
	global_store_dwordx4 v[72:73], v[0:3], off offset:48
	s_nop 1
	v_mov_b32_e32 v0, v94
	s_andn2_b64 exec, exec, s[10:11]
	s_cbranch_execnz .LBB0_762

.LBB0_770:
	s_cmpk_ge_i32 s56, 0x70
	s_cselect_b64 s[10:11], -1, 0
	ds_bpermute_b32 v6, v97, v96
	s_and_b64 vcc, s[10:11], s[48:49]
	v_cndmask_b32_e32 v94, v0, v98, vcc
	v_ashrrev_i32_e32 v95, 31, v94
	s_add_i32 s10, s56, 16
	s_and_b32 s10, s10, 0x70
	v_lshlrev_b64 v[94:95], 9, v[94:95]
	v_lshl_add_u64 v[94:95], s[94:95], 0, v[94:95]
	s_lshl_b32 s36, s10, 2
	s_waitcnt lgkmcnt(0)
	s_waitcnt vmcnt(32)
	v_mov_b32_e32 v96, v122
	v_ashrrev_i32_e32 v7, 31, v6
	v_lshl_add_u64 v[94:95], v[94:95], 0, s[36:37]
	v_lshl_add_u64 v[6:7], v[6:7], 3, s[88:89]
	v_lshl_add_u64 v[94:95], v[94:95], 0, v[144:145]
	global_load_dwordx2 v[6:7], v[6:7], off
	s_nop 0
	global_load_dword v8, v[4:5], off
	global_load_dword v122, v[94:95], off
	s_waitcnt vmcnt(19)
	v_dot8_i32_i4 v9, v20, v1, 0
	v_dot8_i32_i4 v94, v20, v10, 0
	v_dot8_i32_i4 v9, v21, v11, v9
	v_dot8_i32_i4 v94, v21, v12, v94
	v_dot8_i32_i4 v20, v22, v1, 0
	v_dot8_i32_i4 v21, v22, v10, 0
	v_dot8_i32_i4 v20, v23, v11, v20
	v_dot8_i32_i4 v21, v23, v12, v21
	v_lshl_add_u32 v9, v9, 4, v94
	s_add_i32 s56, s56, 16
	s_nop 0
	v_lshl_add_u32 v94, v20, 4, v21
	s_waitcnt vmcnt(19)
	v_dot8_i32_i4 v20, v24, v1, 0
	v_dot8_i32_i4 v21, v24, v10, 0
	v_dot8_i32_i4 v20, v25, v11, v20
	v_dot8_i32_i4 v21, v25, v12, v21
	v_lshl_add_u64 v[4:5], v[4:5], 0, 64
	s_nop 1
	v_lshl_add_u32 v95, v20, 4, v21
	v_dot8_i32_i4 v20, v26, v1, 0
	v_dot8_i32_i4 v21, v26, v10, 0
	v_dot8_i32_i4 v20, v27, v11, v20
	v_dot8_i32_i4 v21, v27, v12, v21
	v_readlane_b32 s10, v96, 0
	s_ashr_i32 s11, s10, 31
	v_readlane_b32 s12, v96, 1
	v_lshl_add_u32 v106, v20, 4, v21
	v_dot8_i32_i4 v20, v28, v1, 0
	v_dot8_i32_i4 v21, v28, v10, 0
	v_dot8_i32_i4 v20, v29, v11, v20
	v_dot8_i32_i4 v21, v29, v12, v21
	s_lshl_b64 s[10:11], s[10:11], 9
	s_ashr_i32 s13, s12, 31
	v_readlane_b32 s14, v96, 2
	v_lshl_add_u32 v107, v20, 4, v21
	v_dot8_i32_i4 v20, v30, v1, 0
	v_dot8_i32_i4 v21, v30, v10, 0
	v_dot8_i32_i4 v20, v31, v11, v20
	v_dot8_i32_i4 v21, v31, v12, v21
	s_lshl_b64 s[12:13], s[12:13], 9
	s_ashr_i32 s15, s14, 31
	v_readlane_b32 s16, v96, 3
	v_lshl_add_u32 v108, v20, 4, v21
	v_dot8_i32_i4 v20, v32, v1, 0
	v_dot8_i32_i4 v21, v32, v10, 0
	v_dot8_i32_i4 v20, v33, v11, v20
	v_dot8_i32_i4 v21, v33, v12, v21
	s_lshl_b64 s[14:15], s[14:15], 9
	s_ashr_i32 s17, s16, 31
	s_nop 0
	v_lshl_add_u32 v109, v20, 4, v21
	v_dot8_i32_i4 v20, v34, v1, 0
	v_dot8_i32_i4 v21, v34, v10, 0
	v_dot8_i32_i4 v20, v35, v11, v20
	v_dot8_i32_i4 v21, v35, v12, v21
	v_readlane_b32 s18, v96, 4
	s_add_u32 s66, s12, s62
	s_addc_u32 s67, s13, s63
	global_load_dwordx2 v[22:23], v121, s[66:67]
	v_lshl_add_u32 v110, v20, 4, v21
	v_dot8_i32_i4 v20, v36, v1, 0
	v_dot8_i32_i4 v21, v36, v10, 0
	v_dot8_i32_i4 v20, v37, v11, v20
	v_dot8_i32_i4 v21, v37, v12, v21
	s_lshl_b64 s[16:17], s[16:17], 9
	s_ashr_i32 s19, s18, 31
	v_readlane_b32 s20, v96, 5
	v_lshl_add_u32 v111, v20, 4, v21
	v_dot8_i32_i4 v20, v38, v1, 0
	v_dot8_i32_i4 v21, v38, v10, 0
	v_dot8_i32_i4 v20, v39, v11, v20
	v_dot8_i32_i4 v21, v39, v12, v21
	s_setprio 2
	v_permlane32_swap_b32 v9, v111
	s_nop 1
	v_lshl_add_u32 v112, v20, 4, v21
	v_dot8_i32_i4 v20, v40, v1, 0
	v_dot8_i32_i4 v21, v40, v10, 0
	v_dot8_i32_i4 v20, v41, v11, v20
	v_dot8_i32_i4 v21, v41, v12, v21
	s_waitcnt lgkmcnt(0)
	v_add_u32_e32 v9, v9, v111
	v_permlane32_swap_b32 v94, v112
	v_lshl_add_u32 v113, v20, 4, v21
	v_dot8_i32_i4 v20, v60, v1, 0
	v_dot8_i32_i4 v21, v60, v10, 0
	v_dot8_i32_i4 v20, v61, v11, v20
	v_dot8_i32_i4 v21, v61, v12, v21
	s_waitcnt lgkmcnt(0)
	v_add_u32_e32 v94, v94, v112
	v_permlane32_swap_b32 v95, v113
	v_lshl_add_u32 v114, v20, 4, v21
	v_dot8_i32_i4 v20, v58, v1, 0
	v_dot8_i32_i4 v21, v58, v10, 0
	v_dot8_i32_i4 v20, v59, v11, v20
	v_dot8_i32_i4 v21, v59, v12, v21
	s_waitcnt lgkmcnt(0)
	v_add_u32_e32 v95, v95, v113
	v_permlane32_swap_b32 v106, v114
	v_lshl_add_u32 v115, v20, 4, v21
	v_dot8_i32_i4 v20, v56, v1, 0
	v_dot8_i32_i4 v21, v56, v10, 0
	v_dot8_i32_i4 v20, v57, v11, v20
	v_dot8_i32_i4 v21, v57, v12, v21
	s_waitcnt lgkmcnt(0)
	v_add_u32_e32 v106, v106, v114
	v_permlane32_swap_b32 v107, v115
	v_lshl_add_u32 v116, v20, 4, v21
	v_dot8_i32_i4 v20, v54, v1, 0
	v_dot8_i32_i4 v21, v54, v10, 0
	v_dot8_i32_i4 v20, v55, v11, v20
	v_dot8_i32_i4 v21, v55, v12, v21
	s_waitcnt lgkmcnt(0)
	v_add_u32_e32 v107, v107, v115
	v_permlane32_swap_b32 v108, v116
	v_lshl_add_u32 v117, v20, 4, v21
	v_dot8_i32_i4 v20, v52, v1, 0
	v_dot8_i32_i4 v21, v52, v10, 0
	v_dot8_i32_i4 v20, v53, v11, v20
	v_dot8_i32_i4 v21, v53, v12, v21
	s_waitcnt lgkmcnt(0)
	v_add_u32_e32 v108, v108, v116
	v_permlane32_swap_b32 v109, v117
	v_lshl_add_u32 v118, v20, 4, v21
	s_waitcnt lgkmcnt(0)
	v_add_u32_e32 v109, v109, v117
	v_permlane32_swap_b32 v110, v118
	s_add_u32 s66, s10, s62
	s_addc_u32 s67, s11, s63
	global_load_dwordx2 v[20:21], v121, s[66:67]
	s_add_u32 s66, s14, s62
	s_addc_u32 s67, s15, s63
	global_load_dwordx2 v[24:25], v121, s[66:67]
	s_waitcnt lgkmcnt(0)
	v_add_u32_e32 v110, v110, v118
	v_permlane16_swap_b32 v9, v107
	s_lshl_b64 s[18:19], s[18:19], 9
	s_ashr_i32 s21, s20, 31
	v_readlane_b32 s22, v96, 6
	s_add_u32 s66, s16, s62
	s_addc_u32 s67, s17, s63
	global_load_dwordx2 v[26:27], v121, s[66:67]
	s_waitcnt lgkmcnt(0)
	v_add_u32_e32 v9, v9, v107
	v_permlane16_swap_b32 v94, v108
	s_lshl_b64 s[20:21], s[20:21], 9
	s_ashr_i32 s23, s22, 31
	s_waitcnt lgkmcnt(0)
	v_add_u32_e32 v94, v94, v108
	v_permlane16_swap_b32 v95, v109
	v_readlane_b32 s24, v96, 7
	s_add_u32 s66, s18, s62
	s_addc_u32 s67, s19, s63
	global_load_dwordx2 v[28:29], v121, s[66:67]
	s_waitcnt lgkmcnt(0)
	v_add_u32_e32 v95, v95, v109
	v_permlane16_swap_b32 v106, v110
	s_lshl_b64 s[22:23], s[22:23], 9
	s_ashr_i32 s25, s24, 31
	v_readlane_b32 s26, v96, 8
	s_waitcnt lgkmcnt(0)
	v_add_u32_e32 v106, v106, v110
	v_cndmask_b32_e64 v107, v9, v95, s[44:45]
	v_cndmask_b32_e64 v9, v95, v9, s[44:45]
	s_nop 0
	s_add_u32 s66, s20, s62
	s_addc_u32 s67, s21, s63
	global_load_dwordx2 v[30:31], v121, s[66:67]
	s_lshl_b64 s[24:25], s[24:25], 9
	s_ashr_i32 s27, s26, 31
	s_waitcnt lgkmcnt(0)
	v_add_u32_dpp v9, v107, v9 row_ror:8 row_mask:0xf bank_mask:0xf
	v_cndmask_b32_e64 v95, v94, v106, s[44:45]
	s_nop 1
	v_cndmask_b32_e64 v94, v106, v94, s[44:45]
	v_readlane_b32 s28, v96, 9
	s_add_u32 s66, s22, s62
	s_addc_u32 s67, s23, s63
	global_load_dwordx2 v[32:33], v121, s[66:67]
	s_waitcnt lgkmcnt(0)
	v_add_u32_dpp v94, v95, v94 row_ror:8 row_mask:0xf bank_mask:0xf
	v_cndmask_b32_e64 v95, v9, v94, s[46:47]
	v_cndmask_b32_e64 v9, v94, v9, s[46:47]
	s_nop 0
	v_mov_b32_dpp v94, v95 row_half_mirror row_mask:0xf bank_mask:0xf
	s_nop 1
	s_lshl_b64 s[26:27], s[26:27], 9
	s_ashr_i32 s29, s28, 31
	v_readlane_b32 s30, v96, 10
	s_add_u32 s66, s24, s62
	s_addc_u32 s67, s25, s63
	global_load_dwordx2 v[34:35], v121, s[66:67]
	s_waitcnt lgkmcnt(0)
	v_add_u32_dpp v9, v94, v9 quad_perm:[3,2,1,0] row_mask:0xf bank_mask:0xf
	s_nop 1
	s_lshl_b64 s[28:29], s[28:29], 9
	s_ashr_i32 s31, s30, 31
	v_readlane_b32 s34, v96, 11
	s_waitcnt lgkmcnt(0)
	v_add_u32_dpp v9, v9, v9 quad_perm:[2,3,0,1] row_mask:0xf bank_mask:0xf
	s_nop 1
	s_add_u32 s66, s26, s62
	s_addc_u32 s67, s27, s63
	global_load_dwordx2 v[36:37], v121, s[66:67]
	s_lshl_b64 s[30:31], s[30:31], 9
	s_ashr_i32 s35, s34, 31
	s_waitcnt lgkmcnt(0)
	v_add_u32_dpp v9, v9, v9 quad_perm:[1,0,3,2] row_mask:0xf bank_mask:0xf
	s_waitcnt vmcnt(10)
	v_mul_f32_e32 v7, v13, v7
	v_cvt_f32_i32_e32 v9, v9
	v_add_f32_e32 v9, v14, v9
	v_mul_f32_e32 v7, v7, v9
	v_mul_f32_e32 v9, 0x3d372713, v7
	v_mul_f32_e32 v9, v7, v9
	v_fma_f32 v9, v7, v9, v7
	v_mul_f32_e32 v9, 0x3fcc422a, v9
	v_mul_f32_e32 v9, 0xbfb8aa3b, v9
	v_exp_f32_e32 v9, v9
	v_readlane_b32 s38, v96, 12
	s_add_u32 s66, s28, s62
	s_addc_u32 s67, s29, s63
	global_load_dwordx2 v[38:39], v121, s[66:67]
	v_add_f32_e32 v9, 1.0, v9
	v_rcp_f32_e32 v9, v9
	s_lshl_b64 s[34:35], s[34:35], 9
	s_ashr_i32 s39, s38, 31
	s_lshl_b64 s[38:39], s[38:39], 9
	v_readlane_b32 s50, v96, 13
	v_readlane_b32 s52, v96, 14
	v_readlane_b32 s54, v96, 15
	s_ashr_i32 s51, s50, 31
	s_ashr_i32 s53, s52, 31
	s_ashr_i32 s55, s54, 31
	s_lshl_b64 s[50:51], s[50:51], 9
	s_lshl_b64 s[52:53], s[52:53], 9
	s_lshl_b64 s[54:55], s[54:55], 9
	s_add_u32 s66, s30, s62
	s_addc_u32 s67, s31, s63
	global_load_dwordx2 v[40:41], v121, s[66:67]
	s_add_u32 s66, s34, s62
	s_addc_u32 s67, s35, s63
	global_load_dwordx2 v[60:61], v121, s[66:67]
	s_add_u32 s66, s38, s62
	s_addc_u32 s67, s39, s63
	global_load_dwordx2 v[58:59], v121, s[66:67]
	s_add_u32 s66, s50, s62
	s_addc_u32 s67, s51, s63
	global_load_dwordx2 v[56:57], v121, s[66:67]
	s_add_u32 s66, s52, s62
	s_addc_u32 s67, s53, s63
	global_load_dwordx2 v[54:55], v121, s[66:67]
	s_add_u32 s66, s54, s62
	s_addc_u32 s67, s55, s63
	global_load_dwordx2 v[52:53], v121, s[66:67]
	v_pk_mul_f32 v[6:7], v[6:7], v[8:9]
	s_waitcnt vmcnt(34)
	v_alignbit_b32 v224, v92, v92, 4
	v_pk_mul_f32 v[6:7], v[6:7], v[6:7] op_sel:[0,1] op_sel_hi:[1,0]
	v_cvt_f16_f32_e32 v120, v6
	s_setprio 0
	v_and_b32_e32 v8, 0x7070707, v92
	v_readlane_b32 s36, v120, 0
	v_and_b32_e32 v9, 0x7070707, v224
	v_perm_b32 v8, s2, v205, v8
	v_perm_b32 v9, s2, v205, v9
	v_and_or_b32 v8, v92, s4, v8
	v_and_or_b32 v9, v224, s4, v9
	v_perm_b32 v92, v9, v8, s5
	v_perm_b32 v94, v9, v8, s33
	v_perm_b32 v95, v9, v8, s0
	v_perm_b32 v8, v9, v8, s1
	v_pk_fma_f16 v8, v8, s36, v102 op_sel_hi:[1,0,1]
	v_alignbit_b32 v225, v93, v93, 4
	v_pk_fma_f16 v9, v92, s36, v105 op_sel_hi:[1,0,1]
	v_pk_fma_f16 v92, v94, s36, v104 op_sel_hi:[1,0,1]
	v_pk_fma_f16 v94, v95, s36, v103 op_sel_hi:[1,0,1]
	v_and_b32_e32 v95, 0x7070707, v93
	v_and_b32_e32 v102, 0x7070707, v225
	v_perm_b32 v95, s2, v205, v95
	v_perm_b32 v102, s2, v205, v102
	v_and_or_b32 v95, v93, s4, v95
	v_and_or_b32 v93, v225, s4, v102
	v_perm_b32 v102, v93, v95, s5
	v_perm_b32 v103, v93, v95, s33
	v_perm_b32 v104, v93, v95, s0
	v_perm_b32 v93, v93, v95, s1
	v_pk_fma_f16 v95, v102, s36, v101 op_sel_hi:[1,0,1]
	v_readlane_b32 s59, v120, 4
	s_waitcnt vmcnt(33)
	v_alignbit_b32 v224, v90, v90, 4
	v_pk_fma_f16 v100, v103, s36, v100 op_sel_hi:[1,0,1]
	v_pk_fma_f16 v99, v104, s36, v99 op_sel_hi:[1,0,1]
	v_pk_fma_f16 v7, v93, s36, v15 op_sel_hi:[1,0,1]
	v_and_b32_e32 v93, 0x7070707, v90
	v_and_b32_e32 v101, 0x7070707, v224
	v_perm_b32 v93, s2, v205, v93
	v_perm_b32 v101, s2, v205, v101
	v_and_or_b32 v93, v90, s4, v93
	v_and_or_b32 v90, v224, s4, v101
	v_perm_b32 v103, v90, v93, s0
	v_perm_b32 v101, v90, v93, s5
	v_perm_b32 v102, v90, v93, s33
	v_perm_b32 v90, v90, v93, s1
	v_pk_fma_f16 v93, v103, s59, v94 op_sel_hi:[1,0,1]
	v_alignbit_b32 v225, v91, v91, 4
	v_pk_fma_f16 v8, v90, s59, v8 op_sel_hi:[1,0,1]
	v_and_b32_e32 v90, 0x7070707, v91
	v_and_b32_e32 v94, 0x7070707, v225
	v_pk_fma_f16 v9, v101, s59, v9 op_sel_hi:[1,0,1]
	v_perm_b32 v90, s2, v205, v90
	v_perm_b32 v94, s2, v205, v94
	v_and_or_b32 v90, v91, s4, v90
	v_and_or_b32 v91, v225, s4, v94
	v_pk_fma_f16 v92, v102, s59, v92 op_sel_hi:[1,0,1]
	v_perm_b32 v94, v91, v90, s5
	v_perm_b32 v102, v91, v90, s0
	v_perm_b32 v101, v91, v90, s33
	v_perm_b32 v90, v91, v90, s1
	v_pk_fma_f16 v91, v94, s59, v95 op_sel_hi:[1,0,1]
	v_pk_fma_f16 v95, v102, s59, v99 op_sel_hi:[1,0,1]
	v_readlane_b32 s60, v120, 8
	s_waitcnt vmcnt(32)
	v_alignbit_b32 v224, v88, v88, 4
	v_pk_fma_f16 v94, v101, s59, v100 op_sel_hi:[1,0,1]
	v_pk_fma_f16 v7, v90, s59, v7 op_sel_hi:[1,0,1]
	v_and_b32_e32 v90, 0x7070707, v88
	v_and_b32_e32 v99, 0x7070707, v224
	v_perm_b32 v90, s2, v205, v90
	v_perm_b32 v99, s2, v205, v99
	v_and_or_b32 v90, v88, s4, v90
	v_and_or_b32 v88, v224, s4, v99
	v_perm_b32 v100, v88, v90, s33
	v_perm_b32 v101, v88, v90, s0
	v_perm_b32 v99, v88, v90, s5
	v_perm_b32 v88, v88, v90, s1
	v_pk_fma_f16 v90, v100, s60, v92 op_sel_hi:[1,0,1]
	v_pk_fma_f16 v92, v101, s60, v93 op_sel_hi:[1,0,1]
	v_alignbit_b32 v225, v89, v89, 4
	v_pk_fma_f16 v8, v88, s60, v8 op_sel_hi:[1,0,1]
	v_and_b32_e32 v88, 0x7070707, v89
	v_and_b32_e32 v93, 0x7070707, v225
	v_pk_fma_f16 v9, v99, s60, v9 op_sel_hi:[1,0,1]
	v_perm_b32 v88, s2, v205, v88
	v_perm_b32 v93, s2, v205, v93
	v_and_or_b32 v88, v89, s4, v88
	v_and_or_b32 v89, v225, s4, v93
	v_perm_b32 v93, v89, v88, s5
	v_perm_b32 v99, v89, v88, s33
	v_perm_b32 v100, v89, v88, s0
	v_perm_b32 v88, v89, v88, s1
	v_pk_fma_f16 v89, v93, s60, v91 op_sel_hi:[1,0,1]
	v_pk_fma_f16 v91, v99, s60, v94 op_sel_hi:[1,0,1]
	v_readlane_b32 s36, v120, 12
	s_waitcnt vmcnt(31)
	v_alignbit_b32 v224, v86, v86, 4
	v_pk_fma_f16 v93, v100, s60, v95 op_sel_hi:[1,0,1]
	v_pk_fma_f16 v7, v88, s60, v7 op_sel_hi:[1,0,1]
	v_and_b32_e32 v88, 0x7070707, v86
	v_and_b32_e32 v94, 0x7070707, v224
	v_perm_b32 v88, s2, v205, v88
	v_perm_b32 v94, s2, v205, v94
	v_and_or_b32 v88, v86, s4, v88
	v_and_or_b32 v86, v224, s4, v94
	v_perm_b32 v95, v86, v88, s33
	v_perm_b32 v99, v86, v88, s0
	v_perm_b32 v94, v86, v88, s5
	v_perm_b32 v86, v86, v88, s1
	v_pk_fma_f16 v88, v95, s36, v90 op_sel_hi:[1,0,1]
	v_pk_fma_f16 v90, v99, s36, v92 op_sel_hi:[1,0,1]
	v_alignbit_b32 v225, v87, v87, 4
	v_pk_fma_f16 v8, v86, s36, v8 op_sel_hi:[1,0,1]
	v_and_b32_e32 v86, 0x7070707, v87
	v_and_b32_e32 v92, 0x7070707, v225
	v_pk_fma_f16 v9, v94, s36, v9 op_sel_hi:[1,0,1]
	v_perm_b32 v86, s2, v205, v86
	v_perm_b32 v92, s2, v205, v92
	v_and_or_b32 v86, v87, s4, v86
	v_and_or_b32 v87, v225, s4, v92
	v_perm_b32 v92, v87, v86, s5
	v_perm_b32 v94, v87, v86, s33
	v_perm_b32 v95, v87, v86, s0
	v_perm_b32 v86, v87, v86, s1
	v_pk_fma_f16 v87, v92, s36, v89 op_sel_hi:[1,0,1]
	v_readlane_b32 s59, v120, 16
	s_waitcnt vmcnt(30)
	v_alignbit_b32 v224, v84, v84, 4
	v_pk_fma_f16 v89, v94, s36, v91 op_sel_hi:[1,0,1]
	v_pk_fma_f16 v91, v95, s36, v93 op_sel_hi:[1,0,1]
	v_pk_fma_f16 v7, v86, s36, v7 op_sel_hi:[1,0,1]
	v_and_b32_e32 v86, 0x7070707, v84
	v_and_b32_e32 v92, 0x7070707, v224
	v_perm_b32 v86, s2, v205, v86
	v_perm_b32 v92, s2, v205, v92
	v_and_or_b32 v86, v84, s4, v86
	v_and_or_b32 v84, v224, s4, v92
	v_perm_b32 v93, v84, v86, s33
	v_perm_b32 v94, v84, v86, s0
	v_perm_b32 v92, v84, v86, s5
	v_perm_b32 v84, v84, v86, s1
	v_pk_fma_f16 v86, v93, s59, v88 op_sel_hi:[1,0,1]
	v_pk_fma_f16 v88, v94, s59, v90 op_sel_hi:[1,0,1]
	v_alignbit_b32 v225, v85, v85, 4
	v_pk_fma_f16 v8, v84, s59, v8 op_sel_hi:[1,0,1]
	v_and_b32_e32 v84, 0x7070707, v85
	v_and_b32_e32 v90, 0x7070707, v225
	v_pk_fma_f16 v9, v92, s59, v9 op_sel_hi:[1,0,1]
	v_perm_b32 v84, s2, v205, v84
	v_perm_b32 v90, s2, v205, v90
	v_and_or_b32 v84, v85, s4, v84
	v_and_or_b32 v85, v225, s4, v90
	v_perm_b32 v90, v85, v84, s5
	v_perm_b32 v92, v85, v84, s33
	v_perm_b32 v93, v85, v84, s0
	v_perm_b32 v84, v85, v84, s1
	v_pk_fma_f16 v85, v90, s59, v87 op_sel_hi:[1,0,1]
	v_readlane_b32 s60, v120, 20
	s_waitcnt vmcnt(29)
	v_alignbit_b32 v224, v82, v82, 4
	v_pk_fma_f16 v87, v92, s59, v89 op_sel_hi:[1,0,1]
	v_pk_fma_f16 v89, v93, s59, v91 op_sel_hi:[1,0,1]
	v_pk_fma_f16 v7, v84, s59, v7 op_sel_hi:[1,0,1]
	v_and_b32_e32 v84, 0x7070707, v82
	v_and_b32_e32 v90, 0x7070707, v224
	v_perm_b32 v84, s2, v205, v84
	v_perm_b32 v90, s2, v205, v90
	v_and_or_b32 v84, v82, s4, v84
	v_and_or_b32 v82, v224, s4, v90
	v_perm_b32 v91, v82, v84, s33
	v_perm_b32 v92, v82, v84, s0
	v_perm_b32 v90, v82, v84, s5
	v_perm_b32 v82, v82, v84, s1
	v_pk_fma_f16 v84, v91, s60, v86 op_sel_hi:[1,0,1]
	v_pk_fma_f16 v86, v92, s60, v88 op_sel_hi:[1,0,1]
	s_add_u32 s66, s10, s64
	s_addc_u32 s67, s11, s65
	global_load_dwordx2 v[92:93], v121, s[66:67]
	v_alignbit_b32 v225, v83, v83, 4
	v_pk_fma_f16 v8, v82, s60, v8 op_sel_hi:[1,0,1]
	v_and_b32_e32 v82, 0x7070707, v83
	v_and_b32_e32 v88, 0x7070707, v225
	v_pk_fma_f16 v9, v90, s60, v9 op_sel_hi:[1,0,1]
	v_perm_b32 v82, s2, v205, v82
	v_perm_b32 v88, s2, v205, v88
	v_and_or_b32 v82, v83, s4, v82
	v_and_or_b32 v83, v225, s4, v88
	v_perm_b32 v88, v83, v82, s5
	v_perm_b32 v90, v83, v82, s33
	v_perm_b32 v91, v83, v82, s0
	v_perm_b32 v82, v83, v82, s1
	v_pk_fma_f16 v83, v88, s60, v85 op_sel_hi:[1,0,1]
	v_readlane_b32 s36, v120, 24
	s_waitcnt vmcnt(29)
	v_alignbit_b32 v224, v80, v80, 4
	v_pk_fma_f16 v85, v90, s60, v87 op_sel_hi:[1,0,1]
	v_pk_fma_f16 v87, v91, s60, v89 op_sel_hi:[1,0,1]
	v_pk_fma_f16 v7, v82, s60, v7 op_sel_hi:[1,0,1]
	v_and_b32_e32 v82, 0x7070707, v80
	v_and_b32_e32 v88, 0x7070707, v224
	v_perm_b32 v82, s2, v205, v82
	v_perm_b32 v88, s2, v205, v88
	v_and_or_b32 v82, v80, s4, v82
	v_and_or_b32 v80, v224, s4, v88
	v_perm_b32 v89, v80, v82, s33
	v_perm_b32 v90, v80, v82, s0
	v_perm_b32 v88, v80, v82, s5
	v_perm_b32 v80, v80, v82, s1
	v_pk_fma_f16 v82, v89, s36, v84 op_sel_hi:[1,0,1]
	v_pk_fma_f16 v84, v90, s36, v86 op_sel_hi:[1,0,1]
	s_add_u32 s66, s12, s64
	s_addc_u32 s67, s13, s65
	global_load_dwordx2 v[90:91], v121, s[66:67]
	v_alignbit_b32 v225, v81, v81, 4
	v_pk_fma_f16 v8, v80, s36, v8 op_sel_hi:[1,0,1]
	v_and_b32_e32 v80, 0x7070707, v81
	v_and_b32_e32 v86, 0x7070707, v225
	v_pk_fma_f16 v9, v88, s36, v9 op_sel_hi:[1,0,1]
	v_perm_b32 v80, s2, v205, v80
	v_perm_b32 v86, s2, v205, v86
	v_and_or_b32 v80, v81, s4, v80
	v_and_or_b32 v81, v225, s4, v86
	v_perm_b32 v86, v81, v80, s5
	v_perm_b32 v88, v81, v80, s33
	v_perm_b32 v89, v81, v80, s0
	v_perm_b32 v80, v81, v80, s1
	v_pk_fma_f16 v81, v86, s36, v83 op_sel_hi:[1,0,1]
	v_readlane_b32 s59, v120, 28
	s_waitcnt vmcnt(29)
	v_alignbit_b32 v224, v78, v78, 4
	v_pk_fma_f16 v83, v88, s36, v85 op_sel_hi:[1,0,1]
	v_pk_fma_f16 v85, v89, s36, v87 op_sel_hi:[1,0,1]
	v_pk_fma_f16 v7, v80, s36, v7 op_sel_hi:[1,0,1]
	v_and_b32_e32 v80, 0x7070707, v78
	v_and_b32_e32 v86, 0x7070707, v224
	v_perm_b32 v80, s2, v205, v80
	v_perm_b32 v86, s2, v205, v86
	v_and_or_b32 v80, v78, s4, v80
	v_and_or_b32 v78, v224, s4, v86
	v_perm_b32 v87, v78, v80, s33
	v_perm_b32 v88, v78, v80, s0
	v_perm_b32 v86, v78, v80, s5
	v_perm_b32 v78, v78, v80, s1
	v_pk_fma_f16 v80, v87, s59, v82 op_sel_hi:[1,0,1]
	v_pk_fma_f16 v82, v88, s59, v84 op_sel_hi:[1,0,1]
	s_add_u32 s66, s14, s64
	s_addc_u32 s67, s15, s65
	global_load_dwordx2 v[88:89], v121, s[66:67]
	v_alignbit_b32 v225, v79, v79, 4
	v_pk_fma_f16 v8, v78, s59, v8 op_sel_hi:[1,0,1]
	v_and_b32_e32 v78, 0x7070707, v79
	v_and_b32_e32 v84, 0x7070707, v225
	v_pk_fma_f16 v9, v86, s59, v9 op_sel_hi:[1,0,1]
	v_perm_b32 v78, s2, v205, v78
	v_perm_b32 v84, s2, v205, v84
	v_and_or_b32 v78, v79, s4, v78
	v_and_or_b32 v79, v225, s4, v84
	v_perm_b32 v84, v79, v78, s5
	v_perm_b32 v86, v79, v78, s33
	v_perm_b32 v87, v79, v78, s0
	v_perm_b32 v78, v79, v78, s1
	v_pk_fma_f16 v79, v84, s59, v81 op_sel_hi:[1,0,1]
	v_readlane_b32 s60, v120, 32
	s_waitcnt vmcnt(29)
	v_alignbit_b32 v224, v76, v76, 4
	v_pk_fma_f16 v81, v86, s59, v83 op_sel_hi:[1,0,1]
	v_pk_fma_f16 v83, v87, s59, v85 op_sel_hi:[1,0,1]
	v_pk_fma_f16 v7, v78, s59, v7 op_sel_hi:[1,0,1]
	v_and_b32_e32 v78, 0x7070707, v76
	v_and_b32_e32 v84, 0x7070707, v224
	v_perm_b32 v78, s2, v205, v78
	v_perm_b32 v84, s2, v205, v84
	v_and_or_b32 v78, v76, s4, v78
	v_and_or_b32 v76, v224, s4, v84
	v_perm_b32 v85, v76, v78, s33
	v_perm_b32 v86, v76, v78, s0
	v_perm_b32 v84, v76, v78, s5
	v_perm_b32 v76, v76, v78, s1
	v_pk_fma_f16 v78, v85, s60, v80 op_sel_hi:[1,0,1]
	v_pk_fma_f16 v80, v86, s60, v82 op_sel_hi:[1,0,1]
	s_add_u32 s66, s16, s64
	s_addc_u32 s67, s17, s65
	global_load_dwordx2 v[86:87], v121, s[66:67]
	v_alignbit_b32 v225, v77, v77, 4
	v_pk_fma_f16 v8, v76, s60, v8 op_sel_hi:[1,0,1]
	v_and_b32_e32 v76, 0x7070707, v77
	v_and_b32_e32 v82, 0x7070707, v225
	v_pk_fma_f16 v9, v84, s60, v9 op_sel_hi:[1,0,1]
	v_perm_b32 v76, s2, v205, v76
	v_perm_b32 v82, s2, v205, v82
	v_and_or_b32 v76, v77, s4, v76
	v_and_or_b32 v77, v225, s4, v82
	v_perm_b32 v82, v77, v76, s5
	v_perm_b32 v84, v77, v76, s33
	v_perm_b32 v85, v77, v76, s0
	v_perm_b32 v76, v77, v76, s1
	v_pk_fma_f16 v77, v82, s60, v79 op_sel_hi:[1,0,1]
	v_readlane_b32 s36, v120, 36
	s_waitcnt vmcnt(28)
	v_alignbit_b32 v224, v70, v70, 4
	v_pk_fma_f16 v79, v84, s60, v81 op_sel_hi:[1,0,1]
	v_pk_fma_f16 v81, v85, s60, v83 op_sel_hi:[1,0,1]
	v_pk_fma_f16 v7, v76, s60, v7 op_sel_hi:[1,0,1]
	v_and_b32_e32 v76, 0x7070707, v70
	v_and_b32_e32 v82, 0x7070707, v224
	v_perm_b32 v76, s2, v205, v76
	v_perm_b32 v82, s2, v205, v82
	v_and_or_b32 v76, v70, s4, v76
	v_and_or_b32 v70, v224, s4, v82
	v_perm_b32 v83, v70, v76, s33
	v_perm_b32 v84, v70, v76, s0
	v_perm_b32 v82, v70, v76, s5
	v_perm_b32 v70, v70, v76, s1
	v_pk_fma_f16 v76, v83, s36, v78 op_sel_hi:[1,0,1]
	v_pk_fma_f16 v78, v84, s36, v80 op_sel_hi:[1,0,1]
	s_add_u32 s66, s18, s64
	s_addc_u32 s67, s19, s65
	global_load_dwordx2 v[84:85], v121, s[66:67]
	v_alignbit_b32 v225, v71, v71, 4
	v_pk_fma_f16 v8, v70, s36, v8 op_sel_hi:[1,0,1]
	v_and_b32_e32 v70, 0x7070707, v71
	v_and_b32_e32 v80, 0x7070707, v225
	v_pk_fma_f16 v9, v82, s36, v9 op_sel_hi:[1,0,1]
	v_perm_b32 v70, s2, v205, v70
	v_perm_b32 v80, s2, v205, v80
	v_and_or_b32 v70, v71, s4, v70
	v_and_or_b32 v71, v225, s4, v80
	v_perm_b32 v80, v71, v70, s5
	v_perm_b32 v82, v71, v70, s33
	v_perm_b32 v83, v71, v70, s0
	v_perm_b32 v70, v71, v70, s1
	v_pk_fma_f16 v71, v80, s36, v77 op_sel_hi:[1,0,1]
	v_readlane_b32 s59, v120, 40
	s_waitcnt vmcnt(25)
	v_alignbit_b32 v224, v66, v66, 4
	v_pk_fma_f16 v77, v82, s36, v79 op_sel_hi:[1,0,1]
	v_pk_fma_f16 v79, v83, s36, v81 op_sel_hi:[1,0,1]
	v_pk_fma_f16 v7, v70, s36, v7 op_sel_hi:[1,0,1]
	v_and_b32_e32 v70, 0x7070707, v66
	v_and_b32_e32 v80, 0x7070707, v224
	v_perm_b32 v70, s2, v205, v70
	v_perm_b32 v80, s2, v205, v80
	v_and_or_b32 v70, v66, s4, v70
	v_and_or_b32 v66, v224, s4, v80
	v_perm_b32 v81, v66, v70, s33
	v_perm_b32 v82, v66, v70, s0
	v_perm_b32 v80, v66, v70, s5
	v_perm_b32 v66, v66, v70, s1
	v_pk_fma_f16 v70, v81, s59, v76 op_sel_hi:[1,0,1]
	v_pk_fma_f16 v76, v82, s59, v78 op_sel_hi:[1,0,1]
	s_add_u32 s66, s20, s64
	s_addc_u32 s67, s21, s65
	global_load_dwordx2 v[82:83], v121, s[66:67]
	v_alignbit_b32 v225, v67, v67, 4
	v_pk_fma_f16 v8, v66, s59, v8 op_sel_hi:[1,0,1]
	v_and_b32_e32 v66, 0x7070707, v67
	v_and_b32_e32 v78, 0x7070707, v225
	v_pk_fma_f16 v9, v80, s59, v9 op_sel_hi:[1,0,1]
	v_perm_b32 v66, s2, v205, v66
	v_perm_b32 v78, s2, v205, v78
	v_and_or_b32 v66, v67, s4, v66
	v_and_or_b32 v67, v225, s4, v78
	v_perm_b32 v78, v67, v66, s5
	v_perm_b32 v80, v67, v66, s33
	v_perm_b32 v81, v67, v66, s0
	v_perm_b32 v66, v67, v66, s1
	v_pk_fma_f16 v67, v78, s59, v71 op_sel_hi:[1,0,1]
	v_readlane_b32 s60, v120, 44
	s_waitcnt vmcnt(31)
	v_alignbit_b32 v224, v72, v72, 4
	v_pk_fma_f16 v71, v80, s59, v77 op_sel_hi:[1,0,1]
	v_pk_fma_f16 v77, v81, s59, v79 op_sel_hi:[1,0,1]
	v_pk_fma_f16 v7, v66, s59, v7 op_sel_hi:[1,0,1]
	v_and_b32_e32 v66, 0x7070707, v72
	v_and_b32_e32 v78, 0x7070707, v224
	v_perm_b32 v66, s2, v205, v66
	v_perm_b32 v78, s2, v205, v78
	v_and_or_b32 v66, v72, s4, v66
	v_and_or_b32 v72, v224, s4, v78
	v_perm_b32 v80, v72, v66, s0
	v_perm_b32 v78, v72, v66, s5
	v_perm_b32 v79, v72, v66, s33
	v_perm_b32 v66, v72, v66, s1
	v_pk_fma_f16 v72, v80, s60, v76 op_sel_hi:[1,0,1]
	s_add_u32 s66, s22, s64
	s_addc_u32 s67, s23, s65
	global_load_dwordx2 v[80:81], v121, s[66:67]
	v_alignbit_b32 v225, v73, v73, 4
	v_pk_fma_f16 v8, v66, s60, v8 op_sel_hi:[1,0,1]
	v_and_b32_e32 v66, 0x7070707, v73
	v_and_b32_e32 v76, 0x7070707, v225
	v_pk_fma_f16 v9, v78, s60, v9 op_sel_hi:[1,0,1]
	v_perm_b32 v66, s2, v205, v66
	v_perm_b32 v76, s2, v205, v76
	v_and_or_b32 v66, v73, s4, v66
	v_and_or_b32 v73, v225, s4, v76
	v_perm_b32 v76, v73, v66, s5
	v_pk_fma_f16 v70, v79, s60, v70 op_sel_hi:[1,0,1]
	v_perm_b32 v78, v73, v66, s33
	v_perm_b32 v79, v73, v66, s0
	v_perm_b32 v66, v73, v66, s1
	v_pk_fma_f16 v67, v76, s60, v67 op_sel_hi:[1,0,1]
	v_readlane_b32 s36, v120, 48
	s_waitcnt vmcnt(30)
	v_alignbit_b32 v224, v68, v68, 4
	v_pk_fma_f16 v71, v78, s60, v71 op_sel_hi:[1,0,1]
	v_pk_fma_f16 v73, v79, s60, v77 op_sel_hi:[1,0,1]
	v_pk_fma_f16 v7, v66, s60, v7 op_sel_hi:[1,0,1]
	v_and_b32_e32 v66, 0x7070707, v68
	v_and_b32_e32 v76, 0x7070707, v224
	v_perm_b32 v66, s2, v205, v66
	v_perm_b32 v76, s2, v205, v76
	v_and_or_b32 v66, v68, s4, v66
	v_and_or_b32 v68, v224, s4, v76
	v_perm_b32 v77, v68, v66, s33
	v_perm_b32 v78, v68, v66, s0
	v_perm_b32 v76, v68, v66, s5
	v_perm_b32 v66, v68, v66, s1
	v_pk_fma_f16 v68, v77, s36, v70 op_sel_hi:[1,0,1]
	v_pk_fma_f16 v70, v78, s36, v72 op_sel_hi:[1,0,1]
	s_add_u32 s66, s24, s64
	s_addc_u32 s67, s25, s65
	global_load_dwordx2 v[78:79], v121, s[66:67]
	v_alignbit_b32 v225, v69, v69, 4
	v_pk_fma_f16 v8, v66, s36, v8 op_sel_hi:[1,0,1]
	v_and_b32_e32 v66, 0x7070707, v69
	v_and_b32_e32 v72, 0x7070707, v225
	v_pk_fma_f16 v9, v76, s36, v9 op_sel_hi:[1,0,1]
	v_perm_b32 v66, s2, v205, v66
	v_perm_b32 v72, s2, v205, v72
	v_and_or_b32 v66, v69, s4, v66
	v_and_or_b32 v69, v225, s4, v72
	v_perm_b32 v72, v69, v66, s5
	v_perm_b32 v76, v69, v66, s33
	v_perm_b32 v77, v69, v66, s0
	v_perm_b32 v66, v69, v66, s1
	v_pk_fma_f16 v67, v72, s36, v67 op_sel_hi:[1,0,1]
	v_readlane_b32 s59, v120, 52
	s_waitcnt vmcnt(29)
	v_alignbit_b32 v224, v64, v64, 4
	v_pk_fma_f16 v69, v76, s36, v71 op_sel_hi:[1,0,1]
	v_pk_fma_f16 v71, v77, s36, v73 op_sel_hi:[1,0,1]
	v_pk_fma_f16 v7, v66, s36, v7 op_sel_hi:[1,0,1]
	v_and_b32_e32 v66, 0x7070707, v64
	v_and_b32_e32 v72, 0x7070707, v224
	v_perm_b32 v66, s2, v205, v66
	v_perm_b32 v72, s2, v205, v72
	v_and_or_b32 v66, v64, s4, v66
	v_and_or_b32 v64, v224, s4, v72
	v_perm_b32 v73, v64, v66, s33
	v_perm_b32 v76, v64, v66, s0
	v_perm_b32 v72, v64, v66, s5
	v_perm_b32 v64, v64, v66, s1
	v_pk_fma_f16 v66, v73, s59, v68 op_sel_hi:[1,0,1]
	v_pk_fma_f16 v68, v76, s59, v70 op_sel_hi:[1,0,1]
	s_add_u32 s66, s26, s64
	s_addc_u32 s67, s27, s65
	global_load_dwordx2 v[76:77], v121, s[66:67]
	v_alignbit_b32 v225, v65, v65, 4
	v_pk_fma_f16 v8, v64, s59, v8 op_sel_hi:[1,0,1]
	v_and_b32_e32 v64, 0x7070707, v65
	v_and_b32_e32 v70, 0x7070707, v225
	v_pk_fma_f16 v9, v72, s59, v9 op_sel_hi:[1,0,1]
	v_perm_b32 v64, s2, v205, v64
	v_perm_b32 v70, s2, v205, v70
	v_and_or_b32 v64, v65, s4, v64
	v_and_or_b32 v65, v225, s4, v70
	v_perm_b32 v70, v65, v64, s5
	v_perm_b32 v72, v65, v64, s33
	v_perm_b32 v73, v65, v64, s0
	v_perm_b32 v64, v65, v64, s1
	v_pk_fma_f16 v65, v70, s59, v67 op_sel_hi:[1,0,1]
	v_readlane_b32 s60, v120, 56
	s_waitcnt vmcnt(31)
	v_alignbit_b32 v224, v62, v62, 4
	v_pk_fma_f16 v67, v72, s59, v69 op_sel_hi:[1,0,1]
	v_pk_fma_f16 v69, v73, s59, v71 op_sel_hi:[1,0,1]
	v_pk_fma_f16 v7, v64, s59, v7 op_sel_hi:[1,0,1]
	v_and_b32_e32 v64, 0x7070707, v62
	v_and_b32_e32 v70, 0x7070707, v224
	v_perm_b32 v64, s2, v205, v64
	v_perm_b32 v70, s2, v205, v70
	v_and_or_b32 v64, v62, s4, v64
	v_and_or_b32 v62, v224, s4, v70
	v_perm_b32 v71, v62, v64, s33
	v_perm_b32 v72, v62, v64, s0
	v_perm_b32 v70, v62, v64, s5
	v_perm_b32 v62, v62, v64, s1
	v_pk_fma_f16 v64, v71, s60, v66 op_sel_hi:[1,0,1]
	v_pk_fma_f16 v66, v72, s60, v68 op_sel_hi:[1,0,1]
	s_add_u32 s66, s34, s64
	s_addc_u32 s67, s35, s65
	global_load_dwordx2 v[72:73], v121, s[66:67]
	v_alignbit_b32 v225, v63, v63, 4
	v_pk_fma_f16 v8, v62, s60, v8 op_sel_hi:[1,0,1]
	v_and_b32_e32 v62, 0x7070707, v63
	v_and_b32_e32 v68, 0x7070707, v225
	v_pk_fma_f16 v9, v70, s60, v9 op_sel_hi:[1,0,1]
	v_perm_b32 v62, s2, v205, v62
	v_perm_b32 v68, s2, v205, v68
	v_and_or_b32 v62, v63, s4, v62
	v_and_or_b32 v63, v225, s4, v68
	v_perm_b32 v68, v63, v62, s5
	v_perm_b32 v70, v63, v62, s33
	v_perm_b32 v71, v63, v62, s0
	v_perm_b32 v62, v63, v62, s1
	v_pk_fma_f16 v7, v62, s60, v7 op_sel_hi:[1,0,1]
	v_readlane_b32 s36, v120, 60
	s_waitcnt vmcnt(29)
	v_alignbit_b32 v224, v50, v50, 4
	v_pk_fma_f16 v63, v68, s60, v65 op_sel_hi:[1,0,1]
	v_pk_fma_f16 v65, v70, s60, v67 op_sel_hi:[1,0,1]
	v_pk_fma_f16 v67, v71, s60, v69 op_sel_hi:[1,0,1]
	s_add_u32 s66, s28, s64
	s_addc_u32 s67, s29, s65
	global_load_dwordx2 v[70:71], v121, s[66:67]
	v_and_b32_e32 v15, 0x7070707, v50
	v_and_b32_e32 v62, 0x7070707, v224
	v_perm_b32 v15, s2, v205, v15
	v_perm_b32 v62, s2, v205, v62
	v_and_or_b32 v15, v50, s4, v15
	v_and_or_b32 v50, v224, s4, v62
	v_perm_b32 v62, v50, v15, s5
	v_perm_b32 v68, v50, v15, s33
	v_perm_b32 v69, v50, v15, s0
	v_perm_b32 v15, v50, v15, s1
	v_pk_fma_f16 v105, v62, s36, v9 op_sel_hi:[1,0,1]
	v_alignbit_b32 v225, v51, v51, 4
	v_pk_fma_f16 v102, v15, s36, v8 op_sel_hi:[1,0,1]
	v_and_b32_e32 v8, 0x7070707, v51
	v_and_b32_e32 v9, 0x7070707, v225
	v_perm_b32 v8, s2, v205, v8
	v_perm_b32 v9, s2, v205, v9
	v_and_or_b32 v8, v51, s4, v8
	v_and_or_b32 v9, v225, s4, v9
	v_perm_b32 v15, v9, v8, s5
	v_perm_b32 v50, v9, v8, s33
	v_perm_b32 v51, v9, v8, s0
	v_perm_b32 v8, v9, v8, s1
	v_pk_fma_f16 v104, v68, s36, v64 op_sel_hi:[1,0,1]
	v_pk_fma_f16 v103, v69, s36, v66 op_sel_hi:[1,0,1]
	s_add_u32 s66, s38, s64
	s_addc_u32 s67, s39, s65
	global_load_dwordx2 v[68:69], v121, s[66:67]
	v_pk_fma_f16 v101, v15, s36, v63 op_sel_hi:[1,0,1]
	s_add_u32 s66, s52, s64
	s_addc_u32 s67, s53, s65
	global_load_dwordx2 v[62:63], v121, s[66:67]
	v_pk_fma_f16 v100, v50, s36, v65 op_sel_hi:[1,0,1]
	s_add_u32 s66, s50, s64
	s_addc_u32 s67, s51, s65
	global_load_dwordx2 v[64:65], v121, s[66:67]
	v_pk_fma_f16 v99, v51, s36, v67 op_sel_hi:[1,0,1]
	s_add_u32 s66, s30, s64
	s_addc_u32 s67, s31, s65
	global_load_dwordx2 v[66:67], v121, s[66:67]
	s_add_u32 s66, s54, s64
	s_addc_u32 s67, s55, s65
	global_load_dwordx2 v[50:51], v121, s[66:67]
	v_pk_fma_f16 v15, v8, s36, v7 op_sel_hi:[1,0,1]
	s_cmpk_eq_i32 s56, 0x90
	s_cbranch_scc0 .LBB0_770
	s_setprio 2
	v_lshl_add_u64 v[94:95], v[2:3], 2, v[44:45]
	v_mov_b32_e32 v106, v208
	v_mov_b32_e32 v107, v209
	v_mov_b32_e32 v108, v210
	v_mov_b32_e32 v109, v211
	v_mov_b32_e32 v8, v212
	v_mov_b32_e32 v9, v213
	v_mov_b32_e32 v10, v214
	v_mov_b32_e32 v11, v215
	v_mov_b32_e32 v4, v216
	v_mov_b32_e32 v5, v217
	v_mov_b32_e32 v6, v218
	v_mov_b32_e32 v7, v219
	v_mov_b32_e32 v0, v220
	v_mov_b32_e32 v1, v221
	v_mov_b32_e32 v2, v222
	v_mov_b32_e32 v3, v223
	v_cvt_f32_f16_sdwa v13, v105 dst_sel:DWORD dst_unused:UNUSED_PAD src0_sel:WORD_1
	v_cvt_f32_f16_e32 v12, v105
	s_mov_b32 s12, 0x800000
	v_readlane_b32 s10, v255, 5
	v_readlane_b32 s11, v255, 6
	v_pk_add_f32 v[0:1], v[0:1], v[12:13]
	v_cvt_f32_f16_sdwa v13, v104 dst_sel:DWORD dst_unused:UNUSED_PAD src0_sel:WORD_1
	v_cvt_f32_f16_e32 v12, v104
	v_lshl_add_u64 v[48:49], v[48:49], 0, s[10:11]
	v_pk_add_f32 v[2:3], v[2:3], v[12:13]
	v_cvt_f32_f16_sdwa v13, v103 dst_sel:DWORD dst_unused:UNUSED_PAD src0_sel:WORD_1
	v_cvt_f32_f16_e32 v12, v103
	global_store_dwordx4 v[94:95], v[0:3], off
	v_pk_add_f32 v[4:5], v[4:5], v[12:13]
	v_cvt_f32_f16_sdwa v13, v102 dst_sel:DWORD dst_unused:UNUSED_PAD src0_sel:WORD_1
	v_cvt_f32_f16_e32 v12, v102
	v_mov_b32_e32 v102, v1
	v_mov_b32_e32 v103, v5
	v_pk_mul_f32 v[102:103], v[102:103], v[102:103]
	v_pk_add_f32 v[6:7], v[6:7], v[12:13]
	v_mov_b32_e32 v12, v0
	v_mov_b32_e32 v13, v4
	v_pk_fma_f32 v[12:13], v[12:13], v[12:13], v[102:103]
	v_mov_b32_e32 v102, v2
	v_mov_b32_e32 v103, v6
	v_pk_fma_f32 v[12:13], v[102:103], v[102:103], v[12:13]
	v_mov_b32_e32 v102, v3
	v_mov_b32_e32 v103, v7
	v_pk_fma_f32 v[102:103], v[102:103], v[102:103], v[12:13]
	v_cvt_f32_f16_sdwa v13, v101 dst_sel:DWORD dst_unused:UNUSED_PAD src0_sel:WORD_1
	v_cvt_f32_f16_e32 v12, v101
	v_cvt_f32_f16_sdwa v101, v15 dst_sel:DWORD dst_unused:UNUSED_PAD src0_sel:WORD_1
	global_store_dwordx4 v[94:95], v[4:7], off offset:16
	v_pk_add_f32 v[8:9], v[8:9], v[12:13]
	v_cvt_f32_f16_sdwa v13, v100 dst_sel:DWORD dst_unused:UNUSED_PAD src0_sel:WORD_1
	v_cvt_f32_f16_e32 v12, v100
	v_cvt_f32_f16_e32 v100, v15
	v_pk_add_f32 v[10:11], v[10:11], v[12:13]
	v_cvt_f32_f16_sdwa v13, v99 dst_sel:DWORD dst_unused:UNUSED_PAD src0_sel:WORD_1
	v_cvt_f32_f16_e32 v12, v99
	v_pk_add_f32 v[14:15], v[108:109], v[100:101]
	v_mov_b32_e32 v100, v9
	global_store_dwordx4 v[94:95], v[8:11], off offset:32
	v_pk_add_f32 v[12:13], v[106:107], v[12:13]
	global_store_dwordx4 v[94:95], v[12:15], off offset:48
	v_mov_b32_e32 v101, v13
	v_mov_b32_e32 v94, v8
	v_mov_b32_e32 v95, v12
	v_pk_mul_f32 v[100:101], v[100:101], v[100:101]
	v_add_f32_e32 v99, v102, v103
	v_pk_fma_f32 v[94:95], v[94:95], v[94:95], v[100:101]
	v_mov_b32_e32 v100, v10
	v_mov_b32_e32 v101, v14
	v_pk_fma_f32 v[94:95], v[100:101], v[100:101], v[94:95]
	v_mov_b32_e32 v100, v11
	v_mov_b32_e32 v101, v15
	v_pk_fma_f32 v[94:95], v[100:101], v[100:101], v[94:95]
	global_load_dwordx4 v[100:103], v[46:47], off offset:48
	global_load_dwordx4 v[104:107], v[46:47], off offset:32
	global_load_dwordx4 v[108:111], v[46:47], off offset:16
	global_load_dwordx4 v[112:115], v[46:47], off
	v_add_f32_e32 v94, v99, v94
	v_add_f32_e32 v94, v94, v95
	v_mov_b32_e32 v95, v94
	s_nop 1
	v_permlane32_swap_b32 v95, v94
	s_waitcnt lgkmcnt(0)
	v_add_f32_e32 v94, v94, v95
	v_mov_b32_e32 v95, v94
	s_nop 1
	v_permlane16_swap_b32 v95, v94
	s_waitcnt lgkmcnt(0)
	v_add_f32_e32 v94, v94, v95
	s_nop 1
	v_mov_b32_dpp v95, v94 row_ror:8 row_mask:0xf bank_mask:0xf
	s_waitcnt lgkmcnt(0)
	v_add_f32_e32 v94, v94, v95
	s_nop 1
	v_mov_b32_dpp v95, v94 row_half_mirror row_mask:0xf bank_mask:0xf
	s_nop 1
	v_mov_b32_dpp v95, v95 quad_perm:[3,2,1,0] row_mask:0xf bank_mask:0xf
	s_waitcnt lgkmcnt(0)
	v_add_f32_e32 v94, v94, v95
	s_nop 1
	v_mov_b32_dpp v95, v94 quad_perm:[2,3,0,1] row_mask:0xf bank_mask:0xf
	s_waitcnt lgkmcnt(0)
	v_add_f32_e32 v94, v94, v95
	s_nop 1
	v_mov_b32_dpp v95, v94 quad_perm:[1,0,3,2] row_mask:0xf bank_mask:0xf
	s_waitcnt lgkmcnt(0)
	v_add_f32_e32 v94, v94, v95
	v_fmamk_f32 v94, v94, 0x3a800000, v191
	v_cmp_gt_f32_e32 vcc, s12, v94
	v_mul_f32_e32 v95, 0x4b800000, v94
	s_nop 0
	v_cndmask_b32_e32 v94, v94, v95, vcc
	v_rsq_f32_e32 v94, v94
	s_nop 0
	v_mul_f32_e32 v95, 0x45800000, v94
	v_cndmask_b32_e32 v94, v94, v95, vcc
	v_pk_mul_f32 v[0:1], v[0:1], v[94:95] op_sel_hi:[1,0]
	v_pk_mul_f32 v[2:3], v[2:3], v[94:95] op_sel_hi:[1,0]
	s_waitcnt vmcnt(0)
	v_pk_mul_f32 v[0:1], v[112:113], v[0:1]
	v_pk_mul_f32 v[2:3], v[114:115], v[2:3]
	v_cvt_pk_bf16_f32 v0, v0, v1
	v_cvt_pk_bf16_f32 v1, v2, v3
	v_pk_mul_f32 v[2:3], v[4:5], v[94:95] op_sel_hi:[1,0]
	v_pk_mul_f32 v[4:5], v[6:7], v[94:95] op_sel_hi:[1,0]
	v_pk_mul_f32 v[2:3], v[108:109], v[2:3]
	v_pk_mul_f32 v[4:5], v[110:111], v[4:5]
	v_cvt_pk_bf16_f32 v2, v2, v3
	v_cvt_pk_bf16_f32 v3, v4, v5
	v_pk_mul_f32 v[4:5], v[8:9], v[94:95] op_sel_hi:[1,0]
	v_pk_mul_f32 v[6:7], v[10:11], v[94:95] op_sel_hi:[1,0]
	v_pk_mul_f32 v[4:5], v[104:105], v[4:5]
	v_pk_mul_f32 v[6:7], v[6:7], v[106:107]
	v_cvt_pk_bf16_f32 v4, v4, v5
	v_cvt_pk_bf16_f32 v5, v6, v7
	v_pk_mul_f32 v[6:7], v[12:13], v[94:95] op_sel_hi:[1,0]
	v_pk_mul_f32 v[8:9], v[14:15], v[94:95] op_sel_hi:[1,0]
	v_pk_mul_f32 v[6:7], v[6:7], v[100:101]
	v_pk_mul_f32 v[8:9], v[8:9], v[102:103]
	v_cvt_pk_bf16_f32 v6, v6, v7
	v_cvt_pk_bf16_f32 v7, v8, v9
	global_store_dwordx4 v[74:75], v[0:3], off
	global_store_dwordx4 v[74:75], v[4:7], off offset:16
	s_nop 0
	v_mov_b32_e32 v0, v98
	s_andn2_b64 exec, exec, s[8:9]
	s_cbranch_execnz .LBB0_769
